# v048 + P5/P15 fmaxf operand canonicalisation self-maxes (160 v_max_f32 vN,vN,vN on arithmetic results) turned into s_nop
# baseline (speedup 1.0000x reference)
.LBB0_415:
	v_mul_f32_e32 v122, v151, v151
	v_mul_f32_e32 v123, v149, v149
	v_fmac_f32_e32 v122, v150, v150
	v_fmac_f32_e32 v123, v148, v148
	v_add_f32_e32 v122, v122, v123
	v_mul_f32_e32 v123, v147, v147
	v_mul_f32_e32 v124, v145, v145
	v_fmac_f32_e32 v123, v146, v146
	v_fmac_f32_e32 v124, v144, v144
	v_add_f32_e32 v123, v123, v124
	v_add_f32_e32 v122, v123, v122
	v_mul_f32_e32 v123, v143, v143
	v_mul_f32_e32 v124, v141, v141
	v_fmac_f32_e32 v123, v142, v142
	v_fmac_f32_e32 v124, v140, v140
	v_add_f32_e32 v123, v123, v124
	v_add_f32_e32 v122, v123, v122
	v_mul_f32_e32 v123, v139, v139
	v_mul_f32_e32 v124, v137, v137
	v_fmac_f32_e32 v123, v138, v138
	v_fmac_f32_e32 v124, v136, v136
	v_add_f32_e32 v123, v123, v124
	v_add_f32_e32 v122, v123, v122
	s_add_i32 s22, s20, s21
	s_add_i32 s0, s22, 16
	v_add_f32_dpp v122, v122, v122 quad_perm:[1,0,3,2] row_mask:0xf bank_mask:0xf bound_ctrl:1
	s_ashr_i32 s1, s0, 31
	s_lshl_b64 s[0:1], s[0:1], 11
	v_add_f32_dpp v122, v122, v122 quad_perm:[2,3,0,1] row_mask:0xf bank_mask:0xf bound_ctrl:1
	v_lshl_add_u64 v[120:121], v[116:117], 0, s[0:1]
	s_add_i32 s18, s22, 17
	v_add_f32_dpp v122, v122, v122 row_half_mirror row_mask:0xf bank_mask:0xf bound_ctrl:1
	s_ashr_i32 s19, s18, 31
	s_ashr_i32 s23, s22, 31
	v_add_f32_dpp v122, v122, v122 row_mirror row_mask:0xf bank_mask:0xf bound_ctrl:1
	v_mov_b32_e32 v123, v122
	s_nop 1
	v_permlane16_swap_b32_e32 v122, v123
	v_add_f32_e32 v122, v122, v123
	v_mov_b32_e32 v123, v122
	s_nop 1
	v_permlane32_swap_b32_e32 v122, v123
	v_add_f32_e32 v122, v122, v123
	v_fmamk_f32 v122, v122, 0x3a800000, v160
	v_mul_f32_e32 v123, 0x4f800000, v122
	v_cmp_gt_f32_e32 vcc, s27, v122
	s_nop 1
	v_cndmask_b32_e32 v128, v122, v123, vcc
	v_sqrt_f32_e32 v129, v128
	global_load_dwordx2 v[126:127], v[120:121], off
	global_load_dwordx2 v[124:125], v[120:121], off offset:512
	global_load_dwordx2 v[122:123], v[120:121], off offset:1024
	s_nop 0
	global_load_dwordx2 v[120:121], v[120:121], off offset:1536
	v_add_u32_e32 v130, -1, v129
	v_fma_f32 v131, -v130, v129, v128
	v_cmp_ge_f32_e64 s[0:1], 0, v131
	v_add_u32_e32 v131, 1, v129
	s_nop 0
	v_cndmask_b32_e64 v130, v129, v130, s[0:1]
	v_fma_f32 v129, -v131, v129, v128
	v_cmp_lt_f32_e64 s[0:1], 0, v129
	s_nop 1
	v_cndmask_b32_e64 v129, v130, v131, s[0:1]
	v_mul_f32_e32 v130, 0x37800000, v129
	v_cndmask_b32_e32 v129, v129, v130, vcc
	v_cmp_class_f32_e32 vcc, v128, v161
	s_nop 1
	v_cndmask_b32_e32 v130, v129, v128, vcc
	v_div_scale_f32 v131, s[0:1], v130, v130, 1.0
	v_rcp_f32_e32 v132, v131
	s_lshl_b64 s[0:1], s[18:19], 11
	v_lshl_add_u64 v[128:129], v[116:117], 0, s[0:1]
	v_fma_f32 v133, -v131, v132, 1.0
	v_fmac_f32_e32 v132, v133, v132
	v_div_scale_f32 v133, vcc, 1.0, v130, 1.0
	v_mul_f32_e32 v134, v133, v132
	v_fma_f32 v135, -v131, v134, v133
	v_fmac_f32_e32 v134, v135, v132
	v_fma_f32 v131, -v131, v134, v133
	v_div_fmas_f32 v131, v131, v132, v134
	v_div_fixup_f32 v130, v131, v130, 1.0
	v_pk_mul_f32 v[132:133], v[130:131], v[150:151] op_sel_hi:[0,1]
	v_pk_mul_f32 v[134:135], v[130:131], v[148:149] op_sel_hi:[0,1]
	v_pk_fma_f32 v[150:151], v[96:97], v[132:133], v[78:79]
	v_pk_mul_f32 v[132:133], v[130:131], v[146:147] op_sel_hi:[0,1]
	v_pk_fma_f32 v[148:149], v[98:99], v[134:135], v[80:81]
	v_pk_mul_f32 v[134:135], v[130:131], v[144:145] op_sel_hi:[0,1]
	v_pk_fma_f32 v[146:147], v[92:93], v[132:133], v[74:75]
	v_pk_mul_f32 v[132:133], v[130:131], v[142:143] op_sel_hi:[0,1]
	v_pk_fma_f32 v[144:145], v[94:95], v[134:135], v[76:77]
	v_pk_mul_f32 v[134:135], v[130:131], v[140:141] op_sel_hi:[0,1]
	v_pk_fma_f32 v[142:143], v[88:89], v[132:133], v[70:71]
	v_pk_mul_f32 v[132:133], v[130:131], v[138:139] op_sel_hi:[0,1]
	v_pk_mul_f32 v[130:131], v[130:131], v[136:137] op_sel_hi:[0,1]
	v_pk_fma_f32 v[136:137], v[86:87], v[130:131], v[68:69]
	v_max_f32_e64 v130, |v148|, |v149|
	v_max_f32_e64 v131, |v144|, |v145|
	v_pk_fma_f32 v[140:141], v[90:91], v[134:135], v[72:73]
	v_max3_f32 v130, |v150|, |v151|, v130
	v_max3_f32 v131, |v146|, |v147|, v131
	v_pk_fma_f32 v[138:139], v[84:85], v[132:133], v[66:67]
	v_max3_f32 v130, v130, 0, v131
	v_max_f32_e64 v131, |v140|, |v141|
	v_max_f32_e64 v132, |v136|, |v137|
	v_max3_f32 v131, |v142|, |v143|, v131
	v_max3_f32 v132, |v138|, |v139|, v132
	v_max3_f32 v130, v130, v131, v132
	s_nop 1
	v_mov_b32_dpp v131, v130 quad_perm:[1,0,3,2] row_mask:0xf bank_mask:0xf bound_ctrl:1
	s_nop 0
	v_max_f32_e32 v130, v130, v131
	s_nop 1
	v_mov_b32_dpp v131, v130 quad_perm:[2,3,0,1] row_mask:0xf bank_mask:0xf bound_ctrl:1
	s_nop 0
	v_max_f32_e32 v130, v130, v131
	s_nop 1
	v_mov_b32_dpp v131, v130 row_half_mirror row_mask:0xf bank_mask:0xf bound_ctrl:1
	s_nop 0
	v_max_f32_e32 v130, v130, v131
	s_nop 1
	v_mov_b32_dpp v131, v130 row_mirror row_mask:0xf bank_mask:0xf bound_ctrl:1
	s_nop 0
	v_max_f32_e32 v130, v130, v131
	v_mov_b32_e32 v131, v130
	s_nop 1
	v_permlane16_swap_b32_e32 v130, v131
	s_nop 0
	s_nop 0
	v_max_f32_e32 v130, v130, v131
	v_mov_b32_e32 v131, v130
	s_nop 1
	v_permlane32_swap_b32_e32 v130, v131
	s_nop 0
	s_nop 0
	v_max_f32_e32 v157, v130, v131
	global_load_dwordx2 v[134:135], v[128:129], off
	global_load_dwordx2 v[132:133], v[128:129], off offset:512
	global_load_dwordx2 v[130:131], v[128:129], off offset:1024
	s_nop 0
	global_load_dwordx2 v[128:129], v[128:129], off offset:1536
	v_div_scale_f32 v163, s[0:1], v157, v157, s28
	v_rcp_f32_e32 v164, v163
	s_lshl_b64 s[0:1], s[22:23], 10
	v_fma_f32 v165, -v163, v164, 1.0
	v_fmac_f32_e32 v164, v165, v164
	v_div_scale_f32 v165, vcc, s28, v157, s28
	v_mul_f32_e32 v166, v165, v164
	v_fma_f32 v167, -v163, v166, v165
	v_fmac_f32_e32 v166, v167, v164
	v_fma_f32 v163, -v163, v166, v165
	v_div_fmas_f32 v163, v163, v164, v166
	v_div_fixup_f32 v163, v163, v157, s28
	v_cmp_lt_f32_e32 vcc, 0, v157
	v_lshl_add_u64 v[164:165], v[118:119], 0, s[0:1]
	s_nop 0
	v_cndmask_b32_e32 v163, 0, v163, vcc
	v_mul_f32_e32 v167, v163, v151
	v_mul_f32_e32 v166, v163, v150
	v_rndne_f32_e32 v167, v167
	v_mul_f32_e32 v168, v163, v148
	v_mul_f32_e32 v169, v163, v149
	v_rndne_f32_e32 v166, v166
	v_rndne_f32_e32 v168, v168
	v_rndne_f32_e32 v169, v169
	v_cvt_i32_f32_e32 v167, v167
	v_cvt_i32_f32_e32 v166, v166
	v_cvt_i32_f32_sdwa v168, v168 dst_sel:WORD_1 dst_unused:UNUSED_PAD src0_sel:DWORD
	v_cvt_i32_f32_e32 v169, v169
	v_lshlrev_b32_e32 v167, 8, v167
	v_and_b32_e32 v167, 0xff00, v167
	v_and_b32_e32 v168, 0xff0000, v168
	v_perm_b32 v166, v169, v166, s29
	v_or3_b32 v166, v166, v167, v168
	v_mul_f32_e32 v167, v163, v147
	global_store_dword v[164:165], v166, off
	v_mul_f32_e32 v166, v163, v146
	v_rndne_f32_e32 v167, v167
	v_mul_f32_e32 v168, v163, v144
	v_mul_f32_e32 v169, v163, v145
	v_rndne_f32_e32 v166, v166
	v_rndne_f32_e32 v168, v168
	v_rndne_f32_e32 v169, v169
	v_cvt_i32_f32_e32 v167, v167
	v_cvt_i32_f32_e32 v166, v166
	v_cvt_i32_f32_sdwa v168, v168 dst_sel:WORD_1 dst_unused:UNUSED_PAD src0_sel:DWORD
	v_cvt_i32_f32_e32 v169, v169
	v_lshlrev_b32_e32 v167, 8, v167
	v_and_b32_e32 v167, 0xff00, v167
	v_and_b32_e32 v168, 0xff0000, v168
	v_perm_b32 v166, v169, v166, s29
	v_or3_b32 v166, v166, v167, v168
	v_mul_f32_e32 v167, v163, v143
	global_store_dword v[164:165], v166, off offset:256
	v_mul_f32_e32 v166, v163, v142
	v_rndne_f32_e32 v167, v167
	v_mul_f32_e32 v168, v163, v140
	v_mul_f32_e32 v169, v163, v141
	v_rndne_f32_e32 v166, v166
	v_rndne_f32_e32 v168, v168
	v_rndne_f32_e32 v169, v169
	v_cvt_i32_f32_e32 v167, v167
	v_cvt_i32_f32_e32 v166, v166
	v_cvt_i32_f32_sdwa v168, v168 dst_sel:WORD_1 dst_unused:UNUSED_PAD src0_sel:DWORD
	v_cvt_i32_f32_e32 v169, v169
	v_lshlrev_b32_e32 v167, 8, v167
	v_and_b32_e32 v167, 0xff00, v167
	v_and_b32_e32 v168, 0xff0000, v168
	v_perm_b32 v166, v169, v166, s29
	v_or3_b32 v166, v166, v167, v168
	v_mul_f32_e32 v167, v163, v139
	global_store_dword v[164:165], v166, off offset:512
	v_mul_f32_e32 v166, v163, v138
	v_rndne_f32_e32 v167, v167
	v_mul_f32_e32 v168, v163, v136
	v_mul_f32_e32 v163, v163, v137
	v_rndne_f32_e32 v166, v166
	v_rndne_f32_e32 v168, v168
	v_rndne_f32_e32 v163, v163
	v_cvt_i32_f32_e32 v167, v167
	v_cvt_i32_f32_e32 v166, v166
	v_cvt_i32_f32_sdwa v168, v168 dst_sel:WORD_1 dst_unused:UNUSED_PAD src0_sel:DWORD
	v_cvt_i32_f32_e32 v163, v163
	v_lshlrev_b32_e32 v167, 8, v167
	v_and_b32_e32 v167, 0xff00, v167
	v_and_b32_e32 v168, 0xff0000, v168
	v_perm_b32 v163, v163, v166, s29
	v_or3_b32 v163, v163, v167, v168
	global_store_dword v[164:165], v163, off offset:768
	s_and_saveexec_b64 s[0:1], s[14:15]
	s_cbranch_execz .LBB0_417
	s_add_i32 s18, s26, 0
	s_add_i32 s30, s18, 0x23500
	s_lshl_b64 s[18:19], s[22:23], 2
	s_add_u32 s18, s82, s18
	s_addc_u32 s19, s83, s19
	v_mul_f32_e32 v157, 0x3c010204, v157
	v_mov_b32_e32 v163, s30
	global_store_dword v83, v157, s[18:19]
	ds_write_b32 v163, v157
.LBB0_417:
	s_or_b64 exec, exec, s[0:1]
	v_cvt_pk_bf16_f32 v164, v150, v151
	v_cvt_pk_bf16_f32 v165, v148, v149
	v_lshlrev_b32_e32 v166, 16, v164
	v_and_b32_e32 v167, 0xffff0000, v164
	v_pk_add_f32 v[150:151], v[150:151], v[166:167] neg_lo:[0,1] neg_hi:[0,1]
	v_lshlrev_b32_e32 v166, 16, v165
	v_and_b32_e32 v167, 0xffff0000, v165
	v_pk_add_f32 v[148:149], v[148:149], v[166:167] neg_lo:[0,1] neg_hi:[0,1]
	v_add_u32_e32 v157, 0, v159
	v_cvt_pk_bf16_f32 v150, v150, v151
	v_cvt_pk_bf16_f32 v151, v148, v149
	v_cvt_pk_bf16_f32 v148, v146, v147
	v_cvt_pk_bf16_f32 v149, v144, v145
	ds_write2st64_b64 v157, v[164:165], v[148:149] offset1:1
	v_lshlrev_b32_e32 v164, 16, v148
	v_and_b32_e32 v165, 0xffff0000, v148
	v_lshlrev_b32_e32 v148, 16, v149
	v_and_b32_e32 v149, 0xffff0000, v149
	v_pk_add_f32 v[146:147], v[146:147], v[164:165] neg_lo:[0,1] neg_hi:[0,1]
	v_pk_add_f32 v[144:145], v[144:145], v[148:149] neg_lo:[0,1] neg_hi:[0,1]
	v_cvt_pk_bf16_f32 v146, v146, v147
	v_cvt_pk_bf16_f32 v147, v144, v145
	v_add_u32_e32 v148, 0x100, v157
	v_cvt_pk_bf16_f32 v144, v142, v143
	ds_write2st64_b64 v148, v[150:151], v[146:147] offset0:64 offset1:65
	v_cvt_pk_bf16_f32 v145, v140, v141
	v_lshlrev_b32_e32 v146, 16, v144
	v_and_b32_e32 v147, 0xffff0000, v144
	v_pk_add_f32 v[142:143], v[142:143], v[146:147] neg_lo:[0,1] neg_hi:[0,1]
	v_lshlrev_b32_e32 v146, 16, v145
	v_and_b32_e32 v147, 0xffff0000, v145
	v_pk_add_f32 v[140:141], v[140:141], v[146:147] neg_lo:[0,1] neg_hi:[0,1]
	v_cvt_pk_bf16_f32 v142, v142, v143
	v_cvt_pk_bf16_f32 v143, v140, v141
	v_cvt_pk_bf16_f32 v140, v138, v139
	v_cvt_pk_bf16_f32 v141, v136, v137
	ds_write2st64_b64 v157, v[144:145], v[140:141] offset0:2 offset1:3
	v_lshlrev_b32_e32 v144, 16, v140
	v_and_b32_e32 v145, 0xffff0000, v140
	v_pk_add_f32 v[138:139], v[138:139], v[144:145] neg_lo:[0,1] neg_hi:[0,1]
	v_mul_f32_e32 v140, v115, v115
	v_mul_f32_e32 v144, v113, v113
	v_fmac_f32_e32 v140, v114, v114
	v_fmac_f32_e32 v144, v112, v112
	v_add_f32_e32 v140, v140, v144
	v_mul_f32_e32 v144, v111, v111
	v_mul_f32_e32 v145, v109, v109
	v_fmac_f32_e32 v144, v110, v110
	v_fmac_f32_e32 v145, v108, v108
	v_add_f32_e32 v144, v144, v145
	v_add_f32_e32 v140, v144, v140
	v_mul_f32_e32 v144, v107, v107
	v_mul_f32_e32 v145, v105, v105
	v_fmac_f32_e32 v144, v106, v106
	v_fmac_f32_e32 v145, v104, v104
	v_add_f32_e32 v144, v144, v145
	v_add_f32_e32 v140, v144, v140
	v_mul_f32_e32 v144, v103, v103
	v_mul_f32_e32 v145, v101, v101
	v_fmac_f32_e32 v144, v102, v102
	v_fmac_f32_e32 v145, v100, v100
	v_add_f32_e32 v144, v144, v145
	v_add_f32_e32 v140, v144, v140
	v_cvt_pk_bf16_f32 v138, v138, v139
	s_nop 0
	v_add_f32_dpp v140, v140, v140 quad_perm:[1,0,3,2] row_mask:0xf bank_mask:0xf bound_ctrl:1
	s_nop 1
	v_add_f32_dpp v140, v140, v140 quad_perm:[2,3,0,1] row_mask:0xf bank_mask:0xf bound_ctrl:1
	s_nop 1
	v_add_f32_dpp v140, v140, v140 row_half_mirror row_mask:0xf bank_mask:0xf bound_ctrl:1
	s_nop 1
	v_add_f32_dpp v140, v140, v140 row_mirror row_mask:0xf bank_mask:0xf bound_ctrl:1
	v_mov_b32_e32 v144, v140
	s_nop 1
	v_permlane16_swap_b32_e32 v140, v144
	v_add_f32_e32 v140, v140, v144
	v_mov_b32_e32 v144, v140
	s_nop 1
	v_permlane32_swap_b32_e32 v140, v144
	v_add_f32_e32 v140, v140, v144
	v_fmamk_f32 v140, v140, 0x3a800000, v160
	v_mul_f32_e32 v144, 0x4f800000, v140
	v_cmp_gt_f32_e32 vcc, s27, v140
	s_nop 1
	v_cndmask_b32_e32 v144, v140, v144, vcc
	v_sqrt_f32_e32 v145, v144
	v_lshlrev_b32_e32 v140, 16, v141
	v_and_b32_e32 v141, 0xffff0000, v141
	v_pk_add_f32 v[136:137], v[136:137], v[140:141] neg_lo:[0,1] neg_hi:[0,1]
	v_add_u32_e32 v139, -1, v145
	v_fma_f32 v146, -v139, v145, v144
	v_cmp_ge_f32_e64 s[0:1], 0, v146
	v_add_u32_e32 v146, 1, v145
	s_nop 0
	v_cndmask_b32_e64 v139, v145, v139, s[0:1]
	v_fma_f32 v145, -v146, v145, v144
	v_cmp_lt_f32_e64 s[0:1], 0, v145
	s_nop 1
	v_cndmask_b32_e64 v139, v139, v146, s[0:1]
	v_mul_f32_e32 v145, 0x37800000, v139
	v_cndmask_b32_e32 v139, v139, v145, vcc
	v_cmp_class_f32_e32 vcc, v144, v161
	s_nop 1
	v_cndmask_b32_e32 v144, v139, v144, vcc
	v_div_scale_f32 v145, s[0:1], v144, v144, 1.0
	v_rcp_f32_e32 v146, v145
	v_cvt_pk_bf16_f32 v139, v136, v137
	ds_write2st64_b64 v148, v[142:143], v[138:139] offset0:66 offset1:67
	v_fma_f32 v136, -v145, v146, 1.0
	v_fmac_f32_e32 v146, v136, v146
	v_div_scale_f32 v136, vcc, 1.0, v144, 1.0
	v_mul_f32_e32 v137, v136, v146
	v_fma_f32 v138, -v145, v137, v136
	v_fmac_f32_e32 v137, v138, v146
	v_fma_f32 v136, -v145, v137, v136
	v_div_fmas_f32 v136, v136, v146, v137
	v_div_fixup_f32 v136, v136, v144, 1.0
	v_pk_mul_f32 v[112:113], v[136:137], v[112:113] op_sel_hi:[0,1]
	v_pk_mul_f32 v[108:109], v[136:137], v[108:109] op_sel_hi:[0,1]
	v_pk_mul_f32 v[114:115], v[136:137], v[114:115] op_sel_hi:[0,1]
	v_pk_fma_f32 v[112:113], v[98:99], v[112:113], v[80:81]
	v_pk_mul_f32 v[110:111], v[136:137], v[110:111] op_sel_hi:[0,1]
	v_pk_fma_f32 v[108:109], v[94:95], v[108:109], v[76:77]
	v_pk_fma_f32 v[114:115], v[96:97], v[114:115], v[78:79]
	v_pk_fma_f32 v[110:111], v[92:93], v[110:111], v[74:75]
	v_pk_mul_f32 v[106:107], v[136:137], v[106:107] op_sel_hi:[0,1]
	v_pk_mul_f32 v[104:105], v[136:137], v[104:105] op_sel_hi:[0,1]
	v_pk_mul_f32 v[102:103], v[136:137], v[102:103] op_sel_hi:[0,1]
	v_pk_mul_f32 v[100:101], v[136:137], v[100:101] op_sel_hi:[0,1]
	v_max_f32_e64 v136, |v112|, |v113|
	v_max_f32_e64 v137, |v108|, |v109|
	v_pk_fma_f32 v[104:105], v[90:91], v[104:105], v[72:73]
	v_pk_fma_f32 v[100:101], v[86:87], v[100:101], v[68:69]
	v_max3_f32 v136, |v114|, |v115|, v136
	v_max3_f32 v137, |v110|, |v111|, v137
	v_pk_fma_f32 v[106:107], v[88:89], v[106:107], v[70:71]
	v_pk_fma_f32 v[102:103], v[84:85], v[102:103], v[66:67]
	v_max3_f32 v136, v136, 0, v137
	v_max_f32_e64 v137, |v104|, |v105|
	v_max_f32_e64 v138, |v100|, |v101|
	v_max3_f32 v137, |v106|, |v107|, v137
	v_max3_f32 v138, |v102|, |v103|, v138
	v_max3_f32 v136, v136, v137, v138
	s_nop 1
	v_mov_b32_dpp v137, v136 quad_perm:[1,0,3,2] row_mask:0xf bank_mask:0xf bound_ctrl:1
	s_nop 0
	v_max_f32_e32 v136, v136, v137
	s_nop 1
	v_mov_b32_dpp v137, v136 quad_perm:[2,3,0,1] row_mask:0xf bank_mask:0xf bound_ctrl:1
	s_nop 0
	v_max_f32_e32 v136, v136, v137
	s_nop 1
	v_mov_b32_dpp v137, v136 row_half_mirror row_mask:0xf bank_mask:0xf bound_ctrl:1
	s_nop 0
	v_max_f32_e32 v136, v136, v137
	s_nop 1
	v_mov_b32_dpp v137, v136 row_mirror row_mask:0xf bank_mask:0xf bound_ctrl:1
	s_nop 0
	v_max_f32_e32 v136, v136, v137
	v_mov_b32_e32 v137, v136
	s_nop 1
	v_permlane16_swap_b32_e32 v136, v137
	s_nop 0
	s_nop 0
	v_max_f32_e32 v136, v136, v137
	v_mov_b32_e32 v137, v136
	s_nop 1
	v_permlane32_swap_b32_e32 v136, v137
	s_nop 0
	s_nop 0
	v_max_f32_e32 v136, v136, v137
	v_div_scale_f32 v137, s[0:1], v136, v136, s28
	v_rcp_f32_e32 v138, v137
	s_add_i32 s0, s22, 1
	s_ashr_i32 s1, s0, 31
	s_lshl_b64 s[18:19], s[0:1], 10
	v_fma_f32 v139, -v137, v138, 1.0
	v_fmac_f32_e32 v138, v139, v138
	v_div_scale_f32 v139, vcc, s28, v136, s28
	v_mul_f32_e32 v140, v139, v138
	v_fma_f32 v141, -v137, v140, v139
	v_fmac_f32_e32 v140, v141, v138
	v_fma_f32 v137, -v137, v140, v139
	v_div_fmas_f32 v137, v137, v138, v140
	v_div_fixup_f32 v137, v137, v136, s28
	v_cmp_lt_f32_e32 vcc, 0, v136
	v_lshl_add_u64 v[138:139], v[118:119], 0, s[18:19]
	s_nop 0
	v_cndmask_b32_e32 v137, 0, v137, vcc
	v_mul_f32_e32 v141, v137, v115
	v_mul_f32_e32 v140, v137, v114
	v_rndne_f32_e32 v141, v141
	v_mul_f32_e32 v142, v137, v112
	v_mul_f32_e32 v143, v137, v113
	v_rndne_f32_e32 v140, v140
	v_rndne_f32_e32 v142, v142
	v_rndne_f32_e32 v143, v143
	v_cvt_i32_f32_e32 v141, v141
	v_cvt_i32_f32_e32 v140, v140
	v_cvt_i32_f32_sdwa v142, v142 dst_sel:WORD_1 dst_unused:UNUSED_PAD src0_sel:DWORD
	v_cvt_i32_f32_e32 v143, v143
	v_lshlrev_b32_e32 v141, 8, v141
	v_and_b32_e32 v141, 0xff00, v141
	v_and_b32_e32 v142, 0xff0000, v142
	v_perm_b32 v140, v143, v140, s29
	v_or3_b32 v140, v140, v141, v142
	v_mul_f32_e32 v141, v137, v111
	global_store_dword v[138:139], v140, off
	v_mul_f32_e32 v140, v137, v110
	v_rndne_f32_e32 v141, v141
	v_mul_f32_e32 v142, v137, v108
	v_mul_f32_e32 v143, v137, v109
	v_rndne_f32_e32 v140, v140
	v_rndne_f32_e32 v142, v142
	v_rndne_f32_e32 v143, v143
	v_cvt_i32_f32_e32 v141, v141
	v_cvt_i32_f32_e32 v140, v140
	v_cvt_i32_f32_sdwa v142, v142 dst_sel:WORD_1 dst_unused:UNUSED_PAD src0_sel:DWORD
	v_cvt_i32_f32_e32 v143, v143
	v_lshlrev_b32_e32 v141, 8, v141
	v_and_b32_e32 v141, 0xff00, v141
	v_and_b32_e32 v142, 0xff0000, v142
	v_perm_b32 v140, v143, v140, s29
	v_or3_b32 v140, v140, v141, v142
	v_mul_f32_e32 v141, v137, v107
	global_store_dword v[138:139], v140, off offset:256
	v_mul_f32_e32 v140, v137, v106
	v_rndne_f32_e32 v141, v141
	v_mul_f32_e32 v142, v137, v104
	v_mul_f32_e32 v143, v137, v105
	v_rndne_f32_e32 v140, v140
	v_rndne_f32_e32 v142, v142
	v_rndne_f32_e32 v143, v143
	v_cvt_i32_f32_e32 v141, v141
	v_cvt_i32_f32_e32 v140, v140
	v_cvt_i32_f32_sdwa v142, v142 dst_sel:WORD_1 dst_unused:UNUSED_PAD src0_sel:DWORD
	v_cvt_i32_f32_e32 v143, v143
	v_lshlrev_b32_e32 v141, 8, v141
	v_and_b32_e32 v141, 0xff00, v141
	v_and_b32_e32 v142, 0xff0000, v142
	v_perm_b32 v140, v143, v140, s29
	v_or3_b32 v140, v140, v141, v142
	v_mul_f32_e32 v141, v137, v103
	global_store_dword v[138:139], v140, off offset:512
	v_mul_f32_e32 v140, v137, v102
	v_rndne_f32_e32 v141, v141
	v_mul_f32_e32 v142, v137, v100
	v_mul_f32_e32 v137, v137, v101
	v_rndne_f32_e32 v140, v140
	v_rndne_f32_e32 v142, v142
	v_rndne_f32_e32 v137, v137
	v_cvt_i32_f32_e32 v141, v141
	v_cvt_i32_f32_e32 v140, v140
	v_cvt_i32_f32_sdwa v142, v142 dst_sel:WORD_1 dst_unused:UNUSED_PAD src0_sel:DWORD
	v_cvt_i32_f32_e32 v137, v137
	v_lshlrev_b32_e32 v141, 8, v141
	v_and_b32_e32 v141, 0xff00, v141
	v_and_b32_e32 v142, 0xff0000, v142
	v_perm_b32 v137, v137, v140, s29
	v_or3_b32 v137, v137, v141, v142
	global_store_dword v[138:139], v137, off offset:768
	s_and_saveexec_b64 s[18:19], s[14:15]
	s_cbranch_execz .LBB0_419
	s_add_i32 s22, s26, 0
	s_add_i32 s22, s22, 0x23504
	s_lshl_b64 s[0:1], s[0:1], 2
	s_add_u32 s0, s82, s0
	s_addc_u32 s1, s83, s1
	v_mul_f32_e32 v136, 0x3c010204, v136
	v_mov_b32_e32 v137, s22
	global_store_dword v83, v136, s[0:1]
	ds_write_b32 v137, v136
.LBB0_419:
	s_or_b64 exec, exec, s[18:19]
	v_cvt_pk_bf16_f32 v136, v114, v115
	v_cvt_pk_bf16_f32 v137, v112, v113
	v_lshlrev_b32_e32 v138, 16, v136
	v_and_b32_e32 v139, 0xffff0000, v136
	v_pk_add_f32 v[114:115], v[114:115], v[138:139] neg_lo:[0,1] neg_hi:[0,1]
	v_lshlrev_b32_e32 v138, 16, v137
	v_and_b32_e32 v139, 0xffff0000, v137
	v_pk_add_f32 v[112:113], v[112:113], v[138:139] neg_lo:[0,1] neg_hi:[0,1]
	v_cvt_pk_bf16_f32 v114, v114, v115
	v_cvt_pk_bf16_f32 v115, v112, v113
	v_cvt_pk_bf16_f32 v112, v110, v111
	v_cvt_pk_bf16_f32 v113, v108, v109
	v_add_u32_e32 v138, 16, v157
	ds_write2st64_b64 v138, v[136:137], v[112:113] offset0:4 offset1:5
	v_lshlrev_b32_e32 v136, 16, v112
	v_and_b32_e32 v137, 0xffff0000, v112
	v_lshlrev_b32_e32 v112, 16, v113
	v_and_b32_e32 v113, 0xffff0000, v113
	v_pk_add_f32 v[110:111], v[110:111], v[136:137] neg_lo:[0,1] neg_hi:[0,1]
	v_pk_add_f32 v[108:109], v[108:109], v[112:113] neg_lo:[0,1] neg_hi:[0,1]
	v_cvt_pk_bf16_f32 v110, v110, v111
	v_cvt_pk_bf16_f32 v111, v108, v109
	v_add_u32_e32 v112, 0x110, v157
	v_cvt_pk_bf16_f32 v108, v106, v107
	ds_write2st64_b64 v112, v[114:115], v[110:111] offset0:68 offset1:69
	v_cvt_pk_bf16_f32 v109, v104, v105
	v_lshlrev_b32_e32 v110, 16, v108
	v_and_b32_e32 v111, 0xffff0000, v108
	v_pk_add_f32 v[106:107], v[106:107], v[110:111] neg_lo:[0,1] neg_hi:[0,1]
	v_lshlrev_b32_e32 v110, 16, v109
	v_and_b32_e32 v111, 0xffff0000, v109
	v_pk_add_f32 v[104:105], v[104:105], v[110:111] neg_lo:[0,1] neg_hi:[0,1]
	v_cvt_pk_bf16_f32 v106, v106, v107
	v_cvt_pk_bf16_f32 v107, v104, v105
	v_cvt_pk_bf16_f32 v104, v102, v103
	v_cvt_pk_bf16_f32 v105, v100, v101
	ds_write2st64_b64 v138, v[108:109], v[104:105] offset0:6 offset1:7
	v_lshlrev_b32_e32 v108, 16, v104
	v_and_b32_e32 v109, 0xffff0000, v104
	v_lshlrev_b32_e32 v104, 16, v105
	v_and_b32_e32 v105, 0xffff0000, v105
	v_pk_add_f32 v[102:103], v[102:103], v[108:109] neg_lo:[0,1] neg_hi:[0,1]
	v_pk_add_f32 v[100:101], v[100:101], v[104:105] neg_lo:[0,1] neg_hi:[0,1]
	v_cvt_pk_bf16_f32 v102, v102, v103
	v_cvt_pk_bf16_f32 v103, v100, v101
	v_add_u32_e32 v163, 0, v158
	ds_write2st64_b64 v112, v[106:107], v[102:103] offset0:70 offset1:71
	s_waitcnt lgkmcnt(0)
	s_barrier
	ds_read_b128 v[100:103], v163
	ds_read_b128 v[104:107], v163 offset:64
	s_waitcnt lgkmcnt(1)
	v_mfma_f32_16x16x32_bf16 v[108:111], v[100:103], v[2:5], 0
	ds_read_b128 v[136:139], v163 offset:33024
	ds_read_b128 v[140:143], v163 offset:33088
	v_mfma_f32_16x16x32_bf16 v[112:115], v[100:103], v[6:9], 0
	s_waitcnt lgkmcnt(1)
	v_mfma_f32_16x16x32_bf16 v[108:111], v[136:139], v[2:5], v[108:111]
	v_mfma_f32_16x16x32_bf16 v[112:115], v[136:139], v[6:9], v[112:115]
	v_mfma_f32_16x16x32_bf16 v[108:111], v[100:103], v[10:13], v[108:111]
	v_mfma_f32_16x16x32_bf16 v[100:103], v[100:103], v[14:17], v[112:115]
	v_mfma_f32_16x16x32_bf16 v[108:111], v[104:107], v[18:21], v[108:111]
	v_mfma_f32_16x16x32_bf16 v[100:103], v[104:107], v[22:25], v[100:103]
	s_waitcnt lgkmcnt(0)
	v_mfma_f32_16x16x32_bf16 v[108:111], v[140:143], v[18:21], v[108:111]
	v_mfma_f32_16x16x32_bf16 v[100:103], v[140:143], v[22:25], v[100:103]
	v_mfma_f32_16x16x32_bf16 v[108:111], v[104:107], v[26:29], v[108:111]
	v_mfma_f32_16x16x32_bf16 v[100:103], v[104:107], v[34:37], v[100:103]
	ds_read_b128 v[104:107], v163 offset:128
	ds_read_b128 v[112:115], v163 offset:192
	ds_read_b128 v[136:139], v163 offset:33152
	ds_read_b128 v[140:143], v163 offset:33216
	s_waitcnt lgkmcnt(3)
	v_mfma_f32_16x16x32_bf16 v[108:111], v[104:107], v[30:33], v[108:111]
	v_mfma_f32_16x16x32_bf16 v[100:103], v[104:107], v[38:41], v[100:103]
	s_waitcnt lgkmcnt(1)
	v_mfma_f32_16x16x32_bf16 v[108:111], v[136:139], v[30:33], v[108:111]
	v_mfma_f32_16x16x32_bf16 v[100:103], v[136:139], v[38:41], v[100:103]
	v_mfma_f32_16x16x32_bf16 v[108:111], v[104:107], v[42:45], v[108:111]
	v_mfma_f32_16x16x32_bf16 v[100:103], v[104:107], v[46:49], v[100:103]
	v_mfma_f32_16x16x32_bf16 v[104:107], v[112:115], v[50:53], v[108:111]
	v_mfma_f32_16x16x32_bf16 v[100:103], v[112:115], v[54:57], v[100:103]
	s_waitcnt lgkmcnt(0)
	v_mfma_f32_16x16x32_bf16 v[104:107], v[140:143], v[50:53], v[104:107]
	v_mfma_f32_16x16x32_bf16 v[100:103], v[140:143], v[54:57], v[100:103]
	v_mfma_f32_16x16x32_bf16 v[104:107], v[112:115], v[58:61], v[104:107]
	v_mfma_f32_16x16x32_bf16 v[100:103], v[112:115], v[62:65], v[100:103]
	s_nop 7
	ds_write2_b32 v156, v104, v100 offset1:16
	ds_write2_b32 v156, v105, v101 offset0:32 offset1:48
	ds_write2_b32 v156, v106, v102 offset0:64 offset1:80
	ds_write2_b32 v156, v107, v103 offset0:96 offset1:112
	s_waitcnt lgkmcnt(0)
	s_barrier
	ds_read2st64_b32 v[100:101], v155 offset1:8
	ds_read2st64_b32 v[102:103], v155 offset0:16 offset1:24
	ds_read2st64_b32 v[104:105], v155 offset0:32 offset1:40
	s_waitcnt lgkmcnt(2)
	v_add_f32_e32 v100, v152, v100
	v_add_f32_e32 v106, v100, v101
	ds_read2st64_b32 v[100:101], v155 offset0:48 offset1:56
	s_waitcnt lgkmcnt(2)
	v_add_f32_e32 v102, v106, v102
	v_add_f32_e32 v102, v102, v103
	s_waitcnt lgkmcnt(1)
	v_add_f32_e32 v102, v102, v104
	v_add_f32_e32 v102, v102, v105
	s_waitcnt lgkmcnt(0)
	v_add_f32_e32 v100, v102, v100
	v_add_f32_e32 v102, v100, v101
	s_nop 1
	v_mov_b32_dpp v100, v102 quad_perm:[1,0,3,2] row_mask:0xf bank_mask:0xf bound_ctrl:1
	s_nop 0
	v_max_f32_e32 v100, v102, v100
	s_nop 1
	v_mov_b32_dpp v101, v100 quad_perm:[2,3,0,1] row_mask:0xf bank_mask:0xf bound_ctrl:1
	s_nop 0
	v_max_f32_e32 v100, v100, v101
	s_nop 1
	v_mov_b32_dpp v101, v100 row_half_mirror row_mask:0xf bank_mask:0xf bound_ctrl:1
	s_nop 0
	v_max_f32_e32 v100, v100, v101
	s_nop 1
	v_mov_b32_dpp v101, v100 row_mirror row_mask:0xf bank_mask:0xf bound_ctrl:1
	s_nop 0
	v_max_f32_e32 v100, v100, v101
	v_mov_b32_e32 v101, v100
	s_nop 1
	v_permlane16_swap_b32_e32 v100, v101
	s_nop 0
	s_nop 0
	v_max_f32_e32 v101, v100, v101
	v_cmp_eq_f32_e32 vcc, v102, v101
	s_nop 1
	v_mov_b32_e32 v100, vcc_hi
	v_mov_b32_e32 v103, vcc_lo
	v_cndmask_b32_e64 v100, v100, v103, s[10:11]
	v_ffbl_b32_e32 v100, v100
	v_cmp_ne_u32_e32 vcc, v1, v100
	s_nop 1
	v_cndmask_b32_e32 v103, v162, v102, vcc
	s_nop 1
	v_mov_b32_dpp v102, v103 quad_perm:[1,0,3,2] row_mask:0xf bank_mask:0xf bound_ctrl:1
	s_nop 0
	v_max_f32_e32 v102, v103, v102
	s_nop 1
	v_mov_b32_dpp v104, v102 quad_perm:[2,3,0,1] row_mask:0xf bank_mask:0xf bound_ctrl:1
	s_nop 0
	v_max_f32_e32 v102, v102, v104
	s_nop 1
	v_mov_b32_dpp v104, v102 row_half_mirror row_mask:0xf bank_mask:0xf bound_ctrl:1
	s_nop 0
	v_max_f32_e32 v102, v102, v104
	s_nop 1
	v_mov_b32_dpp v104, v102 row_mirror row_mask:0xf bank_mask:0xf bound_ctrl:1
	s_nop 0
	v_max_f32_e32 v102, v102, v104
	v_mov_b32_e32 v104, v102
	s_nop 1
	v_permlane16_swap_b32_e32 v102, v104
	s_nop 0
	s_nop 0
	v_max_f32_e32 v104, v102, v104
	v_cmp_eq_f32_e32 vcc, v103, v104
	s_nop 1
	v_mov_b32_e32 v102, vcc_hi
	v_mov_b32_e32 v105, vcc_lo
	v_cndmask_b32_e64 v102, v102, v105, s[10:11]
	v_ffbl_b32_e32 v102, v102
	v_cmp_ne_u32_e32 vcc, v1, v102
	s_nop 1
	v_cndmask_b32_e32 v106, v162, v103, vcc
	s_nop 1
	v_mov_b32_dpp v103, v106 quad_perm:[1,0,3,2] row_mask:0xf bank_mask:0xf bound_ctrl:1
	s_nop 0
	v_max_f32_e32 v103, v106, v103
	s_nop 1
	v_mov_b32_dpp v105, v103 quad_perm:[2,3,0,1] row_mask:0xf bank_mask:0xf bound_ctrl:1
	s_nop 0
	v_max_f32_e32 v103, v103, v105
	s_nop 1
	v_mov_b32_dpp v105, v103 row_half_mirror row_mask:0xf bank_mask:0xf bound_ctrl:1
	s_nop 0
	v_max_f32_e32 v103, v103, v105
	s_nop 1
	v_mov_b32_dpp v105, v103 row_mirror row_mask:0xf bank_mask:0xf bound_ctrl:1
	s_nop 0
	v_max_f32_e32 v103, v103, v105
	v_mov_b32_e32 v105, v103
	s_nop 1
	v_permlane16_swap_b32_e32 v103, v105
	s_nop 0
	s_nop 0
	v_max_f32_e32 v105, v103, v105
	v_cmp_eq_f32_e32 vcc, v106, v105
	s_nop 1
	v_mov_b32_e32 v103, vcc_hi
	v_mov_b32_e32 v107, vcc_lo
	v_cndmask_b32_e64 v103, v103, v107, s[10:11]
	v_ffbl_b32_e32 v103, v103
	v_cmp_ne_u32_e32 vcc, v1, v103
	s_nop 1
	v_cndmask_b32_e32 v107, v162, v106, vcc
	s_nop 1
	v_mov_b32_dpp v106, v107 quad_perm:[1,0,3,2] row_mask:0xf bank_mask:0xf bound_ctrl:1
	s_nop 0
	v_max_f32_e32 v106, v107, v106
	s_nop 1
	v_mov_b32_dpp v108, v106 quad_perm:[2,3,0,1] row_mask:0xf bank_mask:0xf bound_ctrl:1
	s_nop 0
	v_max_f32_e32 v106, v106, v108
	s_nop 1
	v_mov_b32_dpp v108, v106 row_half_mirror row_mask:0xf bank_mask:0xf bound_ctrl:1
	s_nop 0
	v_max_f32_e32 v106, v106, v108
	s_nop 1
	v_mov_b32_dpp v108, v106 row_mirror row_mask:0xf bank_mask:0xf bound_ctrl:1
	s_nop 0
	v_max_f32_e32 v106, v106, v108
	v_mov_b32_e32 v108, v106
	s_nop 1
	v_permlane16_swap_b32_e32 v106, v108
	s_nop 0
	s_nop 0
	v_max_f32_e32 v106, v106, v108
	v_cmp_eq_f32_e64 s[0:1], v107, v106
	s_and_saveexec_b64 s[18:19], s[12:13]
	s_cbranch_execz .LBB0_414
	v_sub_f32_e32 v104, v104, v101
	v_mul_f32_e32 v104, 0x3fb8aa3b, v104
	v_sub_f32_e32 v105, v105, v101
	v_exp_f32_e32 v104, v104
	v_mul_f32_e32 v105, 0x3fb8aa3b, v105
	v_sub_f32_e32 v101, v106, v101
	v_exp_f32_e32 v105, v105
	v_mul_f32_e32 v101, 0x3fb8aa3b, v101
	v_exp_f32_e32 v101, v101
	v_add_f32_e32 v106, 1.0, v104
	v_add_f32_e32 v106, v106, v105
	v_add_f32_e32 v106, v106, v101
	v_div_scale_f32 v107, s[22:23], v106, v106, 1.0
	v_rcp_f32_e32 v108, v107
	v_cndmask_b32_e64 v101, v101, v105, s[8:9]
	v_cndmask_b32_e64 v101, v101, v104, s[6:7]
	v_cndmask_b32_e64 v101, v101, 1.0, s[4:5]
	v_fma_f32 v109, -v107, v108, 1.0
	v_fmac_f32_e32 v108, v109, v108
	v_div_scale_f32 v109, vcc, 1.0, v106, 1.0
	v_mul_f32_e32 v110, v109, v108
	v_fma_f32 v111, -v107, v110, v109
	v_fmac_f32_e32 v110, v111, v108
	v_fma_f32 v107, -v107, v110, v109
	v_div_fmas_f32 v107, v107, v108, v110
	v_div_fixup_f32 v106, v107, v106, 1.0
	v_mov_b32_e32 v107, s1
	v_mov_b32_e32 v108, s0
	v_cndmask_b32_e64 v107, v107, v108, s[10:11]
	v_ffbl_b32_e32 v107, v107
	v_cndmask_b32_e64 v103, v107, v103, s[8:9]
	v_cndmask_b32_e64 v102, v103, v102, s[6:7]
	v_cndmask_b32_e64 v100, v102, v100, s[4:5]
	v_lshl_add_u32 v102, v100, 2, 0
	v_add_u32_e32 v102, 0x20400, v102
	ds_add_rtn_u32 v102, v102, v154
	v_add_u32_e32 v103, 0, v82
	v_add_u32_e32 v104, 0x20500, v103
	ds_write_b32 v104, v100
	v_add_u32_e32 v100, 0x21500, v103
	v_mul_f32_e32 v101, v106, v101
	s_waitcnt lgkmcnt(1)
	ds_write_b32 v100, v102
	v_add_u32_e32 v100, 0x22500, v103
	ds_write_b32 v100, v101
	s_branch .LBB0_414
.LBB0_421:
	v_mul_f32_e32 v82, v151, v151
	v_mul_f32_e32 v83, v149, v149
	v_fmac_f32_e32 v82, v150, v150
	v_fmac_f32_e32 v83, v148, v148
	v_add_f32_e32 v82, v82, v83
	v_mul_f32_e32 v83, v147, v147
	v_mul_f32_e32 v116, v145, v145
	v_fmac_f32_e32 v83, v146, v146
	v_fmac_f32_e32 v116, v144, v144
	v_add_f32_e32 v83, v83, v116
	v_add_f32_e32 v82, v82, v83
	v_mul_f32_e32 v83, v143, v143
	v_mul_f32_e32 v116, v141, v141
	v_fmac_f32_e32 v83, v142, v142
	v_fmac_f32_e32 v116, v140, v140
	v_add_f32_e32 v83, v83, v116
	v_add_f32_e32 v82, v83, v82
	v_mul_f32_e32 v83, v139, v139
	v_mul_f32_e32 v116, v137, v137
	v_fmac_f32_e32 v83, v138, v138
	v_fmac_f32_e32 v116, v136, v136
	v_add_f32_e32 v83, v83, v116
	v_add_f32_e32 v82, v83, v82
	v_mov_b32_e32 v131, 0x358637bd
	s_mov_b32 s21, 0xf800000
	v_add_f32_dpp v82, v82, v82 quad_perm:[1,0,3,2] row_mask:0xf bank_mask:0xf bound_ctrl:1
	v_mov_b32_e32 v132, 0x260
	s_mov_b32 s22, 0x42fe0000
	v_add_f32_dpp v82, v82, v82 quad_perm:[2,3,0,1] row_mask:0xf bank_mask:0xf bound_ctrl:1
	s_add_i32 s23, s25, 0xf0
	s_mov_b32 s20, 0x40c0c00
	v_add_f32_dpp v82, v82, v82 row_half_mirror row_mask:0xf bank_mask:0xf bound_ctrl:1
	s_nop 1
	v_add_f32_dpp v82, v82, v82 row_mirror row_mask:0xf bank_mask:0xf bound_ctrl:1
	v_mov_b32_e32 v83, v82
	s_nop 1
	v_permlane16_swap_b32_e32 v82, v83
	v_add_f32_e32 v82, v82, v83
	v_mov_b32_e32 v83, v82
	s_nop 1
	v_permlane32_swap_b32_e32 v82, v83
	v_add_f32_e32 v82, v82, v83
	v_fmamk_f32 v82, v82, 0x3a800000, v131
	v_mul_f32_e32 v83, 0x4f800000, v82
	v_cmp_gt_f32_e32 vcc, s21, v82
	s_nop 1
	v_cndmask_b32_e32 v82, v82, v83, vcc
	v_sqrt_f32_e32 v83, v82
	s_nop 0
	v_add_u32_e32 v116, -1, v83
	v_fma_f32 v117, -v116, v83, v82
	v_cmp_ge_f32_e64 s[0:1], 0, v117
	v_add_u32_e32 v117, 1, v83
	s_nop 0
	v_cndmask_b32_e64 v116, v83, v116, s[0:1]
	v_fma_f32 v83, -v117, v83, v82
	v_cmp_lt_f32_e64 s[0:1], 0, v83
	s_nop 1
	v_cndmask_b32_e64 v83, v116, v117, s[0:1]
	v_mul_f32_e32 v116, 0x37800000, v83
	v_cndmask_b32_e32 v83, v83, v116, vcc
	v_cmp_class_f32_e32 vcc, v82, v132
	s_nop 1
	v_cndmask_b32_e32 v82, v83, v82, vcc
	v_div_scale_f32 v83, s[0:1], v82, v82, 1.0
	v_rcp_f32_e32 v116, v83
	s_add_i32 s0, s23, s24
	s_ashr_i32 s1, s0, 31
	v_fma_f32 v117, -v83, v116, 1.0
	v_fmac_f32_e32 v116, v117, v116
	v_div_scale_f32 v117, vcc, 1.0, v82, 1.0
	v_mul_f32_e32 v118, v117, v116
	v_fma_f32 v119, -v83, v118, v117
	v_fmac_f32_e32 v118, v119, v116
	v_fma_f32 v83, -v83, v118, v117
	v_div_fmas_f32 v83, v83, v116, v118
	v_div_fixup_f32 v82, v83, v82, 1.0
	v_pk_mul_f32 v[118:119], v[148:149], v[82:83] op_sel_hi:[1,0]
	v_pk_mul_f32 v[116:117], v[150:151], v[82:83] op_sel_hi:[1,0]
	v_pk_fma_f32 v[124:125], v[98:99], v[118:119], v[80:81]
	v_pk_mul_f32 v[118:119], v[144:145], v[82:83] op_sel_hi:[1,0]
	v_pk_fma_f32 v[128:129], v[96:97], v[116:117], v[78:79]
	v_pk_mul_f32 v[116:117], v[146:147], v[82:83] op_sel_hi:[1,0]
	v_pk_fma_f32 v[122:123], v[94:95], v[118:119], v[76:77]
	v_pk_mul_f32 v[118:119], v[142:143], v[82:83] op_sel_hi:[1,0]
	v_pk_fma_f32 v[126:127], v[92:93], v[116:117], v[74:75]
	v_pk_mul_f32 v[116:117], v[140:141], v[82:83] op_sel_hi:[1,0]
	v_pk_fma_f32 v[120:121], v[88:89], v[118:119], v[70:71]
	v_pk_mul_f32 v[118:119], v[138:139], v[82:83] op_sel_hi:[1,0]
	v_pk_mul_f32 v[82:83], v[136:137], v[82:83] op_sel_hi:[1,0]
	v_max_f32_e64 v130, |v124|, |v125|
	v_max_f32_e64 v133, |v122|, |v123|
	v_pk_fma_f32 v[116:117], v[90:91], v[116:117], v[72:73]
	v_pk_fma_f32 v[82:83], v[86:87], v[82:83], v[68:69]
	v_max3_f32 v130, |v128|, |v129|, v130
	v_max3_f32 v133, |v126|, |v127|, v133
	v_pk_fma_f32 v[118:119], v[84:85], v[118:119], v[66:67]
	v_max3_f32 v130, v130, 0, v133
	v_max_f32_e64 v133, |v116|, |v117|
	v_max_f32_e64 v134, |v82|, |v83|
	v_max3_f32 v133, |v120|, |v121|, v133
	v_max3_f32 v134, |v118|, |v119|, v134
	v_max3_f32 v130, v130, v133, v134
	s_nop 1
	v_mov_b32_dpp v133, v130 quad_perm:[1,0,3,2] row_mask:0xf bank_mask:0xf bound_ctrl:1
	s_nop 0
	v_max_f32_e32 v130, v130, v133
	s_nop 1
	v_mov_b32_dpp v133, v130 quad_perm:[2,3,0,1] row_mask:0xf bank_mask:0xf bound_ctrl:1
	s_nop 0
	v_max_f32_e32 v130, v130, v133
	s_nop 1
	v_mov_b32_dpp v133, v130 row_half_mirror row_mask:0xf bank_mask:0xf bound_ctrl:1
	s_nop 0
	v_max_f32_e32 v130, v130, v133
	s_nop 1
	v_mov_b32_dpp v133, v130 row_mirror row_mask:0xf bank_mask:0xf bound_ctrl:1
	s_nop 0
	v_max_f32_e32 v130, v130, v133
	v_mov_b32_e32 v133, v130
	s_nop 1
	v_permlane16_swap_b32_e32 v130, v133
	s_nop 0
	s_nop 0
	v_max_f32_e32 v130, v130, v133
	v_mov_b32_e32 v133, v130
	s_nop 1
	v_permlane32_swap_b32_e32 v130, v133
	s_nop 0
	s_nop 0
	v_max_f32_e32 v133, v130, v133
	v_div_scale_f32 v130, s[18:19], v133, v133, s22
	v_rcp_f32_e32 v134, v130
	s_lshl_b64 s[18:19], s[0:1], 10
	s_add_u32 s18, s96, s18
	s_addc_u32 s19, s97, s19
	v_fma_f32 v135, -v130, v134, 1.0
	v_fmac_f32_e32 v134, v135, v134
	v_div_scale_f32 v135, vcc, s22, v133, s22
	v_mul_f32_e32 v136, v135, v134
	v_fma_f32 v137, -v130, v136, v135
	v_fmac_f32_e32 v136, v137, v134
	v_fma_f32 v130, -v130, v136, v135
	v_div_fmas_f32 v130, v130, v134, v136
	v_div_fixup_f32 v130, v130, v133, s22
	v_cmp_lt_f32_e32 vcc, 0, v133
	s_nop 1
	v_cndmask_b32_e32 v134, 0, v130, vcc
	v_mul_f32_e32 v136, v134, v129
	v_mul_f32_e32 v135, v134, v128
	v_rndne_f32_e32 v136, v136
	v_mul_f32_e32 v137, v134, v124
	v_mul_f32_e32 v138, v134, v125
	v_rndne_f32_e32 v135, v135
	v_rndne_f32_e32 v137, v137
	v_cvt_i32_f32_e32 v136, v136
	v_rndne_f32_e32 v138, v138
	v_cvt_i32_f32_e32 v135, v135
	v_cvt_i32_f32_sdwa v137, v137 dst_sel:WORD_1 dst_unused:UNUSED_PAD src0_sel:DWORD
	v_cvt_i32_f32_e32 v138, v138
	v_lshlrev_b32_e32 v136, 8, v136
	v_and_b32_e32 v136, 0xff00, v136
	v_and_b32_e32 v137, 0xff0000, v137
	v_perm_b32 v135, v138, v135, s20
	v_lshlrev_b32_e32 v130, 2, v174
	v_or3_b32 v135, v135, v136, v137
	v_mul_f32_e32 v136, v134, v127
	global_store_dword v130, v135, s[18:19]
	v_mul_f32_e32 v135, v134, v126
	v_rndne_f32_e32 v136, v136
	v_mul_f32_e32 v137, v134, v122
	v_mul_f32_e32 v138, v134, v123
	v_rndne_f32_e32 v135, v135
	v_rndne_f32_e32 v137, v137
	v_rndne_f32_e32 v138, v138
	v_cvt_i32_f32_e32 v136, v136
	v_cvt_i32_f32_e32 v135, v135
	v_cvt_i32_f32_sdwa v137, v137 dst_sel:WORD_1 dst_unused:UNUSED_PAD src0_sel:DWORD
	v_cvt_i32_f32_e32 v138, v138
	v_lshlrev_b32_e32 v136, 8, v136
	v_and_b32_e32 v136, 0xff00, v136
	v_and_b32_e32 v137, 0xff0000, v137
	v_perm_b32 v135, v138, v135, s20
	v_or3_b32 v135, v135, v136, v137
	v_mul_f32_e32 v136, v134, v121
	global_store_dword v130, v135, s[18:19] offset:256
	v_mul_f32_e32 v135, v134, v120
	v_rndne_f32_e32 v136, v136
	v_mul_f32_e32 v137, v134, v116
	v_mul_f32_e32 v138, v134, v117
	v_rndne_f32_e32 v135, v135
	v_rndne_f32_e32 v137, v137
	v_rndne_f32_e32 v138, v138
	v_cvt_i32_f32_e32 v136, v136
	v_cvt_i32_f32_e32 v135, v135
	v_cvt_i32_f32_sdwa v137, v137 dst_sel:WORD_1 dst_unused:UNUSED_PAD src0_sel:DWORD
	v_cvt_i32_f32_e32 v138, v138
	v_lshlrev_b32_e32 v136, 8, v136
	v_and_b32_e32 v136, 0xff00, v136
	v_and_b32_e32 v137, 0xff0000, v137
	v_perm_b32 v135, v138, v135, s20
	v_or3_b32 v135, v135, v136, v137
	v_mul_f32_e32 v136, v134, v119
	global_store_dword v130, v135, s[18:19] offset:512
	v_mul_f32_e32 v135, v134, v118
	v_rndne_f32_e32 v136, v136
	v_mul_f32_e32 v137, v134, v82
	v_mul_f32_e32 v134, v134, v83
	v_rndne_f32_e32 v135, v135
	v_rndne_f32_e32 v137, v137
	v_rndne_f32_e32 v134, v134
	v_cvt_i32_f32_e32 v136, v136
	v_cvt_i32_f32_e32 v135, v135
	v_cvt_i32_f32_sdwa v137, v137 dst_sel:WORD_1 dst_unused:UNUSED_PAD src0_sel:DWORD
	v_cvt_i32_f32_e32 v134, v134
	v_lshlrev_b32_e32 v136, 8, v136
	v_and_b32_e32 v136, 0xff00, v136
	v_and_b32_e32 v137, 0xff0000, v137
	v_perm_b32 v134, v134, v135, s20
	v_or3_b32 v134, v134, v136, v137
	global_store_dword v130, v134, s[18:19] offset:768
	s_and_saveexec_b64 s[18:19], s[14:15]
	s_cbranch_execz .LBB0_423
	s_lshl_b32 s23, s23, 2
	s_add_i32 s23, s23, 0
	s_add_i32 s23, s23, 0x23500
	s_lshl_b64 s[0:1], s[0:1], 2
	s_add_u32 s0, s82, s0
	s_addc_u32 s1, s83, s1
	v_mov_b32_e32 v134, 0
	v_mul_f32_e32 v133, 0x3c010204, v133
	global_store_dword v134, v133, s[0:1]
	v_mov_b32_e32 v134, s23
	ds_write_b32 v134, v133
.LBB0_423:
	s_or_b64 exec, exec, s[18:19]
	v_cvt_pk_bf16_f32 v134, v128, v129
	v_cvt_pk_bf16_f32 v135, v124, v125
	v_lshlrev_b32_e32 v136, 16, v134
	v_and_b32_e32 v137, 0xffff0000, v134
	v_pk_add_f32 v[128:129], v[128:129], v[136:137] neg_lo:[0,1] neg_hi:[0,1]
	v_lshlrev_b32_e32 v136, 16, v135
	v_and_b32_e32 v137, 0xffff0000, v135
	v_pk_add_f32 v[124:125], v[124:125], v[136:137] neg_lo:[0,1] neg_hi:[0,1]
	v_cvt_pk_bf16_f32 v128, v128, v129
	v_cvt_pk_bf16_f32 v129, v124, v125
	v_cvt_pk_bf16_f32 v124, v126, v127
	v_cvt_pk_bf16_f32 v125, v122, v123
	ds_write2st64_b64 v157, v[134:135], v[124:125] offset1:1
	v_lshlrev_b32_e32 v134, 16, v124
	v_and_b32_e32 v135, 0xffff0000, v124
	v_pk_add_f32 v[126:127], v[126:127], v[134:135] neg_lo:[0,1] neg_hi:[0,1]
	s_nop 0
	v_cvt_pk_bf16_f32 v124, v126, v127
	v_lshlrev_b32_e32 v126, 16, v125
	v_and_b32_e32 v127, 0xffff0000, v125
	v_pk_add_f32 v[122:123], v[122:123], v[126:127] neg_lo:[0,1] neg_hi:[0,1]
	v_add_u32_e32 v126, 0x100, v157
	v_cvt_pk_bf16_f32 v125, v122, v123
	v_cvt_pk_bf16_f32 v122, v120, v121
	ds_write2st64_b64 v126, v[128:129], v[124:125] offset0:64 offset1:65
	v_cvt_pk_bf16_f32 v123, v116, v117
	v_lshlrev_b32_e32 v124, 16, v122
	v_and_b32_e32 v125, 0xffff0000, v122
	v_pk_add_f32 v[120:121], v[120:121], v[124:125] neg_lo:[0,1] neg_hi:[0,1]
	v_lshlrev_b32_e32 v124, 16, v123
	v_and_b32_e32 v125, 0xffff0000, v123
	v_pk_add_f32 v[116:117], v[116:117], v[124:125] neg_lo:[0,1] neg_hi:[0,1]
	v_cvt_pk_bf16_f32 v120, v120, v121
	v_cvt_pk_bf16_f32 v121, v116, v117
	v_cvt_pk_bf16_f32 v116, v118, v119
	v_cvt_pk_bf16_f32 v117, v82, v83
	ds_write2st64_b64 v157, v[122:123], v[116:117] offset0:2 offset1:3
	v_lshlrev_b32_e32 v122, 16, v116
	v_and_b32_e32 v123, 0xffff0000, v116
	v_pk_add_f32 v[118:119], v[118:119], v[122:123] neg_lo:[0,1] neg_hi:[0,1]
	v_mul_f32_e32 v122, v113, v113
	v_cvt_pk_bf16_f32 v116, v118, v119
	v_mul_f32_e32 v119, v115, v115
	v_fmac_f32_e32 v119, v114, v114
	v_fmac_f32_e32 v122, v112, v112
	v_add_f32_e32 v119, v119, v122
	v_mul_f32_e32 v122, v111, v111
	v_mul_f32_e32 v123, v109, v109
	v_fmac_f32_e32 v122, v110, v110
	v_fmac_f32_e32 v123, v108, v108
	v_add_f32_e32 v122, v122, v123
	v_add_f32_e32 v119, v119, v122
	v_mul_f32_e32 v122, v107, v107
	v_mul_f32_e32 v123, v105, v105
	v_fmac_f32_e32 v122, v106, v106
	v_fmac_f32_e32 v123, v104, v104
	v_add_f32_e32 v122, v122, v123
	v_add_f32_e32 v119, v122, v119
	v_mul_f32_e32 v122, v103, v103
	v_mul_f32_e32 v123, v101, v101
	v_fmac_f32_e32 v122, v102, v102
	v_fmac_f32_e32 v123, v100, v100
	v_add_f32_e32 v122, v122, v123
	v_add_f32_e32 v119, v122, v119
	v_lshlrev_b32_e32 v118, 16, v117
	s_nop 0
	v_add_f32_dpp v119, v119, v119 quad_perm:[1,0,3,2] row_mask:0xf bank_mask:0xf bound_ctrl:1
	s_nop 1
	v_add_f32_dpp v119, v119, v119 quad_perm:[2,3,0,1] row_mask:0xf bank_mask:0xf bound_ctrl:1
	s_nop 1
	v_add_f32_dpp v119, v119, v119 row_half_mirror row_mask:0xf bank_mask:0xf bound_ctrl:1
	s_nop 1
	v_add_f32_dpp v119, v119, v119 row_mirror row_mask:0xf bank_mask:0xf bound_ctrl:1
	v_mov_b32_e32 v122, v119
	s_nop 1
	v_permlane16_swap_b32_e32 v119, v122
	v_add_f32_e32 v119, v119, v122
	v_mov_b32_e32 v122, v119
	s_nop 1
	v_permlane32_swap_b32_e32 v119, v122
	v_add_f32_e32 v119, v119, v122
	v_fmac_f32_e32 v131, 0x3a800000, v119
	v_mul_f32_e32 v119, 0x4f800000, v131
	v_cmp_gt_f32_e32 vcc, s21, v131
	s_add_i32 s21, s25, 0xf1
	s_nop 0
	v_cndmask_b32_e32 v122, v131, v119, vcc
	v_sqrt_f32_e32 v123, v122
	v_and_b32_e32 v119, 0xffff0000, v117
	v_pk_add_f32 v[82:83], v[82:83], v[118:119] neg_lo:[0,1] neg_hi:[0,1]
	s_nop 0
	v_cvt_pk_bf16_f32 v117, v82, v83
	v_add_u32_e32 v82, -1, v123
	v_fma_f32 v83, -v82, v123, v122
	v_cmp_ge_f32_e64 s[0:1], 0, v83
	v_add_u32_e32 v83, 1, v123
	v_fma_f32 v118, -v83, v123, v122
	v_cndmask_b32_e64 v82, v123, v82, s[0:1]
	v_cmp_lt_f32_e64 s[0:1], 0, v118
	ds_write2st64_b64 v126, v[120:121], v[116:117] offset0:66 offset1:67
	s_nop 0
	v_cndmask_b32_e64 v82, v82, v83, s[0:1]
	v_mul_f32_e32 v83, 0x37800000, v82
	v_cndmask_b32_e32 v82, v82, v83, vcc
	v_cmp_class_f32_e32 vcc, v122, v132
	s_nop 1
	v_cndmask_b32_e32 v82, v82, v122, vcc
	v_div_scale_f32 v83, s[0:1], v82, v82, 1.0
	v_rcp_f32_e32 v118, v83
	s_add_i32 s0, s21, s24
	s_ashr_i32 s1, s0, 31
	v_fma_f32 v116, -v83, v118, 1.0
	v_fmac_f32_e32 v118, v116, v118
	v_div_scale_f32 v116, vcc, 1.0, v82, 1.0
	v_mul_f32_e32 v117, v116, v118
	v_fma_f32 v119, -v83, v117, v116
	v_fmac_f32_e32 v117, v119, v118
	v_fma_f32 v83, -v83, v117, v116
	v_div_fmas_f32 v83, v83, v118, v117
	v_div_fixup_f32 v82, v83, v82, 1.0
	v_pk_mul_f32 v[114:115], v[114:115], v[82:83] op_sel_hi:[1,0]
	v_pk_mul_f32 v[112:113], v[112:113], v[82:83] op_sel_hi:[1,0]
	v_pk_fma_f32 v[78:79], v[96:97], v[114:115], v[78:79]
	v_pk_mul_f32 v[96:97], v[110:111], v[82:83] op_sel_hi:[1,0]
	v_pk_fma_f32 v[80:81], v[98:99], v[112:113], v[80:81]
	v_pk_mul_f32 v[98:99], v[108:109], v[82:83] op_sel_hi:[1,0]
	v_pk_fma_f32 v[74:75], v[92:93], v[96:97], v[74:75]
	v_pk_mul_f32 v[92:93], v[106:107], v[82:83] op_sel_hi:[1,0]
	v_pk_fma_f32 v[76:77], v[94:95], v[98:99], v[76:77]
	v_pk_mul_f32 v[94:95], v[104:105], v[82:83] op_sel_hi:[1,0]
	v_pk_fma_f32 v[70:71], v[88:89], v[92:93], v[70:71]
	v_pk_mul_f32 v[88:89], v[102:103], v[82:83] op_sel_hi:[1,0]
	v_pk_mul_f32 v[82:83], v[100:101], v[82:83] op_sel_hi:[1,0]
	v_pk_fma_f32 v[72:73], v[90:91], v[94:95], v[72:73]
	v_pk_fma_f32 v[68:69], v[86:87], v[82:83], v[68:69]
	v_max_f32_e64 v82, |v80|, |v81|
	v_max_f32_e64 v83, |v76|, |v77|
	v_max3_f32 v82, |v78|, |v79|, v82
	v_max3_f32 v83, |v74|, |v75|, v83
	v_pk_fma_f32 v[66:67], v[84:85], v[88:89], v[66:67]
	v_max3_f32 v82, v82, 0, v83
	v_max_f32_e64 v83, |v72|, |v73|
	v_max_f32_e64 v84, |v68|, |v69|
	v_max3_f32 v83, |v70|, |v71|, v83
	v_max3_f32 v84, |v66|, |v67|, v84
	v_max3_f32 v82, v82, v83, v84
	s_nop 1
	v_mov_b32_dpp v83, v82 quad_perm:[1,0,3,2] row_mask:0xf bank_mask:0xf bound_ctrl:1
	s_nop 0
	v_max_f32_e32 v82, v82, v83
	s_nop 1
	v_mov_b32_dpp v83, v82 quad_perm:[2,3,0,1] row_mask:0xf bank_mask:0xf bound_ctrl:1
	s_nop 0
	v_max_f32_e32 v82, v82, v83
	s_nop 1
	v_mov_b32_dpp v83, v82 row_half_mirror row_mask:0xf bank_mask:0xf bound_ctrl:1
	s_nop 0
	v_max_f32_e32 v82, v82, v83
	s_nop 1
	v_mov_b32_dpp v83, v82 row_mirror row_mask:0xf bank_mask:0xf bound_ctrl:1
	s_nop 0
	v_max_f32_e32 v82, v82, v83
	v_mov_b32_e32 v83, v82
	s_nop 1
	v_permlane16_swap_b32_e32 v82, v83
	s_nop 0
	s_nop 0
	v_max_f32_e32 v82, v82, v83
	v_mov_b32_e32 v83, v82
	s_nop 1
	v_permlane32_swap_b32_e32 v82, v83
	s_nop 0
	s_nop 0
	v_max_f32_e32 v82, v82, v83
	v_div_scale_f32 v83, s[18:19], v82, v82, s22
	v_rcp_f32_e32 v84, v83
	s_lshl_b64 s[18:19], s[0:1], 10
	s_add_u32 s18, s96, s18
	s_addc_u32 s19, s97, s19
	v_fma_f32 v85, -v83, v84, 1.0
	v_fmac_f32_e32 v84, v85, v84
	v_div_scale_f32 v85, vcc, s22, v82, s22
	v_mul_f32_e32 v86, v85, v84
	v_fma_f32 v87, -v83, v86, v85
	v_fmac_f32_e32 v86, v87, v84
	v_fma_f32 v83, -v83, v86, v85
	v_div_fmas_f32 v83, v83, v84, v86
	v_div_fixup_f32 v83, v83, v82, s22
	v_cmp_lt_f32_e32 vcc, 0, v82
	s_nop 1
	v_cndmask_b32_e32 v83, 0, v83, vcc
	v_mul_f32_e32 v85, v83, v79
	v_mul_f32_e32 v84, v83, v78
	v_rndne_f32_e32 v85, v85
	v_mul_f32_e32 v86, v83, v80
	v_mul_f32_e32 v87, v83, v81
	v_rndne_f32_e32 v84, v84
	v_rndne_f32_e32 v86, v86
	v_rndne_f32_e32 v87, v87
	v_cvt_i32_f32_e32 v85, v85
	v_cvt_i32_f32_e32 v84, v84
	v_cvt_i32_f32_sdwa v86, v86 dst_sel:WORD_1 dst_unused:UNUSED_PAD src0_sel:DWORD
	v_cvt_i32_f32_e32 v87, v87
	v_lshlrev_b32_e32 v85, 8, v85
	v_and_b32_e32 v85, 0xff00, v85
	v_and_b32_e32 v86, 0xff0000, v86
	v_perm_b32 v84, v87, v84, s20
	v_or3_b32 v84, v84, v85, v86
	v_mul_f32_e32 v85, v83, v75
	global_store_dword v130, v84, s[18:19]
	v_mul_f32_e32 v84, v83, v74
	v_rndne_f32_e32 v85, v85
	v_mul_f32_e32 v86, v83, v76
	v_mul_f32_e32 v87, v83, v77
	v_rndne_f32_e32 v84, v84
	v_rndne_f32_e32 v86, v86
	v_rndne_f32_e32 v87, v87
	v_cvt_i32_f32_e32 v85, v85
	v_cvt_i32_f32_e32 v84, v84
	v_cvt_i32_f32_sdwa v86, v86 dst_sel:WORD_1 dst_unused:UNUSED_PAD src0_sel:DWORD
	v_cvt_i32_f32_e32 v87, v87
	v_lshlrev_b32_e32 v85, 8, v85
	v_and_b32_e32 v85, 0xff00, v85
	v_and_b32_e32 v86, 0xff0000, v86
	v_perm_b32 v84, v87, v84, s20
	v_or3_b32 v84, v84, v85, v86
	v_mul_f32_e32 v85, v83, v71
	global_store_dword v130, v84, s[18:19] offset:256
	v_mul_f32_e32 v84, v83, v70
	v_rndne_f32_e32 v85, v85
	v_mul_f32_e32 v86, v83, v72
	v_mul_f32_e32 v87, v83, v73
	v_rndne_f32_e32 v84, v84
	v_rndne_f32_e32 v86, v86
	v_rndne_f32_e32 v87, v87
	v_cvt_i32_f32_e32 v85, v85
	v_cvt_i32_f32_e32 v84, v84
	v_cvt_i32_f32_sdwa v86, v86 dst_sel:WORD_1 dst_unused:UNUSED_PAD src0_sel:DWORD
	v_cvt_i32_f32_e32 v87, v87
	v_lshlrev_b32_e32 v85, 8, v85
	v_and_b32_e32 v85, 0xff00, v85
	v_and_b32_e32 v86, 0xff0000, v86
	v_perm_b32 v84, v87, v84, s20
	v_or3_b32 v84, v84, v85, v86
	v_mul_f32_e32 v85, v83, v67
	global_store_dword v130, v84, s[18:19] offset:512
	v_mul_f32_e32 v84, v83, v66
	v_rndne_f32_e32 v85, v85
	v_mul_f32_e32 v86, v83, v68
	v_mul_f32_e32 v83, v83, v69
	v_rndne_f32_e32 v84, v84
	v_rndne_f32_e32 v86, v86
	v_rndne_f32_e32 v83, v83
	v_cvt_i32_f32_e32 v85, v85
	v_cvt_i32_f32_e32 v84, v84
	v_cvt_i32_f32_sdwa v86, v86 dst_sel:WORD_1 dst_unused:UNUSED_PAD src0_sel:DWORD
	v_cvt_i32_f32_e32 v83, v83
	v_lshlrev_b32_e32 v85, 8, v85
	v_and_b32_e32 v85, 0xff00, v85
	v_and_b32_e32 v86, 0xff0000, v86
	v_perm_b32 v83, v83, v84, s20
	v_or3_b32 v83, v83, v85, v86
	global_store_dword v130, v83, s[18:19] offset:768
	s_and_saveexec_b64 s[18:19], s[14:15]
	s_cbranch_execz .LBB0_425
	s_lshl_b32 s14, s21, 2
	s_add_i32 s14, s14, 0
	s_add_i32 s14, s14, 0x23500
	s_lshl_b64 s[0:1], s[0:1], 2
	s_add_u32 s0, s82, s0
	s_addc_u32 s1, s83, s1
	v_mov_b32_e32 v83, 0
	v_mul_f32_e32 v82, 0x3c010204, v82
	global_store_dword v83, v82, s[0:1]
	v_mov_b32_e32 v83, s14
	ds_write_b32 v83, v82
.LBB0_425:
	s_or_b64 exec, exec, s[18:19]
	v_cvt_pk_bf16_f32 v82, v78, v79
	v_cvt_pk_bf16_f32 v83, v80, v81
	v_lshlrev_b32_e32 v84, 16, v82
	v_and_b32_e32 v85, 0xffff0000, v82
	v_pk_add_f32 v[78:79], v[78:79], v[84:85] neg_lo:[0,1] neg_hi:[0,1]
	v_lshlrev_b32_e32 v84, 16, v83
	v_and_b32_e32 v85, 0xffff0000, v83
	v_pk_add_f32 v[80:81], v[80:81], v[84:85] neg_lo:[0,1] neg_hi:[0,1]
	v_cvt_pk_bf16_f32 v78, v78, v79
	v_cvt_pk_bf16_f32 v79, v80, v81
	v_cvt_pk_bf16_f32 v80, v74, v75
	v_cvt_pk_bf16_f32 v81, v76, v77
	v_add_u32_e32 v84, 16, v157
	ds_write2st64_b64 v84, v[82:83], v[80:81] offset0:4 offset1:5
	v_lshlrev_b32_e32 v82, 16, v80
	v_and_b32_e32 v83, 0xffff0000, v80
	v_lshlrev_b32_e32 v80, 16, v81
	v_and_b32_e32 v81, 0xffff0000, v81
	v_pk_add_f32 v[74:75], v[74:75], v[82:83] neg_lo:[0,1] neg_hi:[0,1]
	v_pk_add_f32 v[76:77], v[76:77], v[80:81] neg_lo:[0,1] neg_hi:[0,1]
	v_cvt_pk_bf16_f32 v74, v74, v75
	v_cvt_pk_bf16_f32 v75, v76, v77
	v_add_u32_e32 v80, 0x110, v157
	ds_write2st64_b64 v80, v[78:79], v[74:75] offset0:68 offset1:69
	v_cvt_pk_bf16_f32 v74, v70, v71
	v_cvt_pk_bf16_f32 v75, v72, v73
	v_lshlrev_b32_e32 v76, 16, v74
	v_and_b32_e32 v77, 0xffff0000, v74
	v_pk_add_f32 v[70:71], v[70:71], v[76:77] neg_lo:[0,1] neg_hi:[0,1]
	v_lshlrev_b32_e32 v76, 16, v75
	v_and_b32_e32 v77, 0xffff0000, v75
	v_pk_add_f32 v[72:73], v[72:73], v[76:77] neg_lo:[0,1] neg_hi:[0,1]
	v_cvt_pk_bf16_f32 v70, v70, v71
	v_cvt_pk_bf16_f32 v71, v72, v73
	v_cvt_pk_bf16_f32 v72, v66, v67
	v_cvt_pk_bf16_f32 v73, v68, v69
	ds_write2st64_b64 v84, v[74:75], v[72:73] offset0:6 offset1:7
	v_lshlrev_b32_e32 v74, 16, v72
	v_and_b32_e32 v75, 0xffff0000, v72
	v_lshlrev_b32_e32 v72, 16, v73
	v_and_b32_e32 v73, 0xffff0000, v73
	v_pk_add_f32 v[66:67], v[66:67], v[74:75] neg_lo:[0,1] neg_hi:[0,1]
	v_pk_add_f32 v[68:69], v[68:69], v[72:73] neg_lo:[0,1] neg_hi:[0,1]
	v_cvt_pk_bf16_f32 v66, v66, v67
	v_cvt_pk_bf16_f32 v67, v68, v69
	ds_write2st64_b64 v80, v[70:71], v[66:67] offset0:70 offset1:71
	s_waitcnt lgkmcnt(0)
	s_barrier
	ds_read_b128 v[66:69], v163
	ds_read_b128 v[70:73], v163 offset:64
	s_waitcnt lgkmcnt(1)
	v_mfma_f32_16x16x32_bf16 v[74:77], v[66:69], v[2:5], 0
	ds_read_b128 v[82:85], v163 offset:33024
	ds_read_b128 v[86:89], v163 offset:33088
	v_mfma_f32_16x16x32_bf16 v[78:81], v[66:69], v[6:9], 0
	s_waitcnt lgkmcnt(1)
	v_mfma_f32_16x16x32_bf16 v[2:5], v[82:85], v[2:5], v[74:77]
	v_mfma_f32_16x16x32_bf16 v[6:9], v[82:85], v[6:9], v[78:81]
	v_mfma_f32_16x16x32_bf16 v[2:5], v[66:69], v[10:13], v[2:5]
	v_mfma_f32_16x16x32_bf16 v[6:9], v[66:69], v[14:17], v[6:9]
	ds_read_b128 v[10:13], v163 offset:128
	ds_read_b128 v[14:17], v163 offset:192
	v_mfma_f32_16x16x32_bf16 v[2:5], v[70:73], v[18:21], v[2:5]
	v_mfma_f32_16x16x32_bf16 v[6:9], v[70:73], v[22:25], v[6:9]
	s_waitcnt lgkmcnt(2)
	v_mfma_f32_16x16x32_bf16 v[2:5], v[86:89], v[18:21], v[2:5]
	v_mfma_f32_16x16x32_bf16 v[6:9], v[86:89], v[22:25], v[6:9]
	ds_read_b128 v[18:21], v163 offset:33152
	ds_read_b128 v[22:25], v163 offset:33216
	v_mfma_f32_16x16x32_bf16 v[2:5], v[70:73], v[26:29], v[2:5]
	v_mfma_f32_16x16x32_bf16 v[6:9], v[70:73], v[34:37], v[6:9]
	s_waitcnt lgkmcnt(3)
	v_mfma_f32_16x16x32_bf16 v[2:5], v[10:13], v[30:33], v[2:5]
	v_mfma_f32_16x16x32_bf16 v[6:9], v[10:13], v[38:41], v[6:9]
	s_waitcnt lgkmcnt(1)
	v_mfma_f32_16x16x32_bf16 v[2:5], v[18:21], v[30:33], v[2:5]
	v_mfma_f32_16x16x32_bf16 v[6:9], v[18:21], v[38:41], v[6:9]
	v_mfma_f32_16x16x32_bf16 v[2:5], v[10:13], v[42:45], v[2:5]
	v_mfma_f32_16x16x32_bf16 v[6:9], v[10:13], v[46:49], v[6:9]
	v_mfma_f32_16x16x32_bf16 v[2:5], v[14:17], v[50:53], v[2:5]
	v_mfma_f32_16x16x32_bf16 v[6:9], v[14:17], v[54:57], v[6:9]
	s_waitcnt lgkmcnt(0)
	v_mfma_f32_16x16x32_bf16 v[2:5], v[22:25], v[50:53], v[2:5]
	v_mfma_f32_16x16x32_bf16 v[6:9], v[22:25], v[54:57], v[6:9]
	v_mfma_f32_16x16x32_bf16 v[2:5], v[14:17], v[58:61], v[2:5]
	v_mfma_f32_16x16x32_bf16 v[6:9], v[14:17], v[62:65], v[6:9]
	s_nop 7
	ds_write2_b32 v156, v2, v6 offset1:16
	ds_write2_b32 v156, v3, v7 offset0:32 offset1:48
	ds_write2_b32 v156, v4, v8 offset0:64 offset1:80
	ds_write2_b32 v156, v5, v9 offset0:96 offset1:112
	s_waitcnt lgkmcnt(0)
	s_barrier
	ds_read2st64_b32 v[2:3], v155 offset1:8
	ds_read2st64_b32 v[4:5], v155 offset0:16 offset1:24
	ds_read2st64_b32 v[6:7], v155 offset0:32 offset1:40
	s_waitcnt lgkmcnt(2)
	v_add_f32_e32 v2, v152, v2
	v_add_f32_e32 v8, v2, v3
	ds_read2st64_b32 v[2:3], v155 offset0:48 offset1:56
	s_waitcnt lgkmcnt(2)
	v_add_f32_e32 v4, v8, v4
	v_add_f32_e32 v4, v4, v5
	s_waitcnt lgkmcnt(1)
	v_add_f32_e32 v4, v4, v6
	v_add_f32_e32 v4, v4, v7
	s_waitcnt lgkmcnt(0)
	v_add_f32_e32 v2, v4, v2
	v_add_f32_e32 v4, v2, v3
	v_mov_b32_e32 v8, 0xff800000
	s_nop 0
	v_mov_b32_dpp v2, v4 quad_perm:[1,0,3,2] row_mask:0xf bank_mask:0xf bound_ctrl:1
	s_nop 0
	v_max_f32_e32 v2, v4, v2
	s_nop 1
	v_mov_b32_dpp v3, v2 quad_perm:[2,3,0,1] row_mask:0xf bank_mask:0xf bound_ctrl:1
	s_nop 0
	v_max_f32_e32 v2, v2, v3
	s_nop 1
	v_mov_b32_dpp v3, v2 row_half_mirror row_mask:0xf bank_mask:0xf bound_ctrl:1
	s_nop 0
	v_max_f32_e32 v2, v2, v3
	s_nop 1
	v_mov_b32_dpp v3, v2 row_mirror row_mask:0xf bank_mask:0xf bound_ctrl:1
	s_nop 0
	v_max_f32_e32 v2, v2, v3
	v_mov_b32_e32 v3, v2
	s_nop 1
	v_permlane16_swap_b32_e32 v2, v3
	s_nop 0
	s_nop 0
	v_max_f32_e32 v3, v2, v3
	v_cmp_eq_f32_e32 vcc, v4, v3
	s_nop 1
	v_mov_b32_e32 v2, vcc_hi
	v_mov_b32_e32 v5, vcc_lo
	v_cndmask_b32_e64 v2, v2, v5, s[10:11]
	v_ffbl_b32_e32 v2, v2
	v_cmp_ne_u32_e32 vcc, v1, v2
	s_nop 1
	v_cndmask_b32_e32 v5, v8, v4, vcc
	s_nop 1
	v_mov_b32_dpp v4, v5 quad_perm:[1,0,3,2] row_mask:0xf bank_mask:0xf bound_ctrl:1
	s_nop 0
	v_max_f32_e32 v4, v5, v4
	s_nop 1
	v_mov_b32_dpp v6, v4 quad_perm:[2,3,0,1] row_mask:0xf bank_mask:0xf bound_ctrl:1
	s_nop 0
	v_max_f32_e32 v4, v4, v6
	s_nop 1
	v_mov_b32_dpp v6, v4 row_half_mirror row_mask:0xf bank_mask:0xf bound_ctrl:1
	s_nop 0
	v_max_f32_e32 v4, v4, v6
	s_nop 1
	v_mov_b32_dpp v6, v4 row_mirror row_mask:0xf bank_mask:0xf bound_ctrl:1
	s_nop 0
	v_max_f32_e32 v4, v4, v6
	v_mov_b32_e32 v6, v4
	s_nop 1
	v_permlane16_swap_b32_e32 v4, v6
	s_nop 0
	s_nop 0
	v_max_f32_e32 v6, v4, v6
	v_cmp_eq_f32_e32 vcc, v5, v6
	s_nop 1
	v_mov_b32_e32 v4, vcc_hi
	v_mov_b32_e32 v7, vcc_lo
	v_cndmask_b32_e64 v4, v4, v7, s[10:11]
	v_ffbl_b32_e32 v4, v4
	v_cmp_ne_u32_e32 vcc, v1, v4
	s_nop 1
	v_cndmask_b32_e32 v9, v8, v5, vcc
	s_nop 1
	v_mov_b32_dpp v5, v9 quad_perm:[1,0,3,2] row_mask:0xf bank_mask:0xf bound_ctrl:1
	s_nop 0
	v_max_f32_e32 v5, v9, v5
	s_nop 1
	v_mov_b32_dpp v7, v5 quad_perm:[2,3,0,1] row_mask:0xf bank_mask:0xf bound_ctrl:1
	s_nop 0
	v_max_f32_e32 v5, v5, v7
	s_nop 1
	v_mov_b32_dpp v7, v5 row_half_mirror row_mask:0xf bank_mask:0xf bound_ctrl:1
	s_nop 0
	v_max_f32_e32 v5, v5, v7
	s_nop 1
	v_mov_b32_dpp v7, v5 row_mirror row_mask:0xf bank_mask:0xf bound_ctrl:1
	s_nop 0
	v_max_f32_e32 v5, v5, v7
	v_mov_b32_e32 v7, v5
	s_nop 1
	v_permlane16_swap_b32_e32 v5, v7
	s_nop 0
	s_nop 0
	v_max_f32_e32 v7, v5, v7
	v_cmp_eq_f32_e32 vcc, v9, v7
	s_nop 1
	v_mov_b32_e32 v5, vcc_hi
	v_mov_b32_e32 v10, vcc_lo
	v_cndmask_b32_e64 v5, v5, v10, s[10:11]
	v_ffbl_b32_e32 v5, v5
	v_cmp_ne_u32_e32 vcc, v1, v5
	s_nop 1
	v_cndmask_b32_e32 v9, v8, v9, vcc
	s_nop 1
	v_mov_b32_dpp v8, v9 quad_perm:[1,0,3,2] row_mask:0xf bank_mask:0xf bound_ctrl:1
	s_nop 0
	v_max_f32_e32 v8, v9, v8
	s_nop 1
	v_mov_b32_dpp v10, v8 quad_perm:[2,3,0,1] row_mask:0xf bank_mask:0xf bound_ctrl:1
	s_nop 0
	v_max_f32_e32 v8, v8, v10
	s_nop 1
	v_mov_b32_dpp v10, v8 row_half_mirror row_mask:0xf bank_mask:0xf bound_ctrl:1
	s_nop 0
	v_max_f32_e32 v8, v8, v10
	s_nop 1
	v_mov_b32_dpp v10, v8 row_mirror row_mask:0xf bank_mask:0xf bound_ctrl:1
	s_nop 0
	v_max_f32_e32 v8, v8, v10
	v_mov_b32_e32 v10, v8
	s_nop 1
	v_permlane16_swap_b32_e32 v8, v10
	s_nop 0
	s_nop 0
	v_max_f32_e32 v8, v8, v10
	v_cmp_eq_f32_e64 s[0:1], v9, v8
	s_and_saveexec_b64 s[14:15], s[12:13]
	s_cbranch_execz .LBB0_427
	v_sub_f32_e32 v6, v6, v3
	v_mul_f32_e32 v6, 0x3fb8aa3b, v6
	v_sub_f32_e32 v7, v7, v3
	v_exp_f32_e32 v6, v6
	v_mul_f32_e32 v7, 0x3fb8aa3b, v7
	v_sub_f32_e32 v3, v8, v3
	v_exp_f32_e32 v7, v7
	v_mul_f32_e32 v3, 0x3fb8aa3b, v3
	v_exp_f32_e32 v3, v3
	v_add_f32_e32 v8, 1.0, v6
	v_add_f32_e32 v8, v8, v7
	v_lshl_add_u32 v1, v153, 2, v1
	v_add_f32_e32 v8, v8, v3
	v_div_scale_f32 v9, s[12:13], v8, v8, 1.0
	v_rcp_f32_e32 v10, v9
	v_cndmask_b32_e64 v3, v3, v7, s[8:9]
	v_cndmask_b32_e64 v3, v3, v6, s[6:7]
	v_lshl_add_u32 v1, v1, 2, 0
	v_fma_f32 v11, -v9, v10, 1.0
	v_fmac_f32_e32 v10, v11, v10
	v_div_scale_f32 v11, vcc, 1.0, v8, 1.0
	v_mul_f32_e32 v12, v11, v10
	v_fma_f32 v13, -v9, v12, v11
	v_fmac_f32_e32 v12, v13, v10
	v_fma_f32 v9, -v9, v12, v11
	v_div_fmas_f32 v9, v9, v10, v12
	v_div_fixup_f32 v8, v9, v8, 1.0
	v_mov_b32_e32 v9, s1
	v_mov_b32_e32 v10, s0
	v_cndmask_b32_e64 v9, v9, v10, s[10:11]
	v_ffbl_b32_e32 v9, v9
	v_cndmask_b32_e64 v5, v9, v5, s[8:9]
	v_cndmask_b32_e64 v4, v5, v4, s[6:7]
	v_cndmask_b32_e64 v2, v4, v2, s[4:5]
	v_lshl_add_u32 v4, v2, 2, 0
	v_add_u32_e32 v4, 0x20400, v4
	v_mov_b32_e32 v5, 1
	ds_add_rtn_u32 v4, v4, v5
	v_cndmask_b32_e64 v3, v3, 1.0, s[4:5]
	v_add_u32_e32 v5, 0x21400, v1
	v_mul_f32_e32 v3, v8, v3
	ds_write_b32 v5, v2
	v_add_u32_e32 v2, 0x22400, v1
	v_add_u32_e32 v1, 0x23400, v1
	s_waitcnt lgkmcnt(1)
	ds_write_b32 v2, v4
	ds_write_b32 v1, v3

.LBB0_2987:
	v_mul_f32_e32 v122, v151, v151
	v_mul_f32_e32 v123, v149, v149
	v_fmac_f32_e32 v122, v150, v150
	v_fmac_f32_e32 v123, v148, v148
	v_add_f32_e32 v122, v122, v123
	v_mul_f32_e32 v123, v147, v147
	v_mul_f32_e32 v124, v145, v145
	v_fmac_f32_e32 v123, v146, v146
	v_fmac_f32_e32 v124, v144, v144
	v_add_f32_e32 v123, v123, v124
	v_add_f32_e32 v122, v123, v122
	v_mul_f32_e32 v123, v143, v143
	v_mul_f32_e32 v124, v141, v141
	v_fmac_f32_e32 v123, v142, v142
	v_fmac_f32_e32 v124, v140, v140
	v_add_f32_e32 v123, v123, v124
	v_add_f32_e32 v122, v123, v122
	v_mul_f32_e32 v123, v139, v139
	v_mul_f32_e32 v124, v137, v137
	v_fmac_f32_e32 v123, v138, v138
	v_fmac_f32_e32 v124, v136, v136
	v_add_f32_e32 v123, v123, v124
	v_add_f32_e32 v122, v123, v122
	s_add_i32 s18, s20, s21
	s_add_i32 s0, s18, 16
	v_add_f32_dpp v122, v122, v122 quad_perm:[1,0,3,2] row_mask:0xf bank_mask:0xf bound_ctrl:1
	s_ashr_i32 s1, s0, 31
	s_lshl_b64 s[0:1], s[0:1], 11
	v_add_f32_dpp v122, v122, v122 quad_perm:[2,3,0,1] row_mask:0xf bank_mask:0xf bound_ctrl:1
	v_lshl_add_u64 v[120:121], v[116:117], 0, s[0:1]
	s_add_i32 s28, s18, 17
	v_add_f32_dpp v122, v122, v122 row_half_mirror row_mask:0xf bank_mask:0xf bound_ctrl:1
	s_ashr_i32 s29, s28, 31
	s_ashr_i32 s19, s18, 31
	v_add_f32_dpp v122, v122, v122 row_mirror row_mask:0xf bank_mask:0xf bound_ctrl:1
	v_mov_b32_e32 v123, v122
	s_nop 1
	v_permlane16_swap_b32_e32 v122, v123
	v_add_f32_e32 v122, v122, v123
	v_mov_b32_e32 v123, v122
	s_nop 1
	v_permlane32_swap_b32_e32 v122, v123
	v_add_f32_e32 v122, v122, v123
	v_fmamk_f32 v122, v122, 0x3a800000, v159
	v_mul_f32_e32 v123, 0x4f800000, v122
	v_cmp_gt_f32_e32 vcc, s25, v122
	s_nop 1
	v_cndmask_b32_e32 v128, v122, v123, vcc
	v_sqrt_f32_e32 v129, v128
	global_load_dwordx2 v[126:127], v[120:121], off
	global_load_dwordx2 v[124:125], v[120:121], off offset:512
	global_load_dwordx2 v[122:123], v[120:121], off offset:1024
	s_nop 0
	global_load_dwordx2 v[120:121], v[120:121], off offset:1536
	v_add_u32_e32 v130, -1, v129
	v_fma_f32 v131, -v130, v129, v128
	v_cmp_ge_f32_e64 s[0:1], 0, v131
	v_add_u32_e32 v131, 1, v129
	s_nop 0
	v_cndmask_b32_e64 v130, v129, v130, s[0:1]
	v_fma_f32 v129, -v131, v129, v128
	v_cmp_lt_f32_e64 s[0:1], 0, v129
	s_nop 1
	v_cndmask_b32_e64 v129, v130, v131, s[0:1]
	v_mul_f32_e32 v130, 0x37800000, v129
	v_cndmask_b32_e32 v129, v129, v130, vcc
	v_cmp_class_f32_e32 vcc, v128, v160
	s_nop 1
	v_cndmask_b32_e32 v130, v129, v128, vcc
	v_div_scale_f32 v131, s[0:1], v130, v130, 1.0
	v_rcp_f32_e32 v132, v131
	s_lshl_b64 s[0:1], s[28:29], 11
	v_lshl_add_u64 v[128:129], v[116:117], 0, s[0:1]
	v_fma_f32 v133, -v131, v132, 1.0
	v_fmac_f32_e32 v132, v133, v132
	v_div_scale_f32 v133, vcc, 1.0, v130, 1.0
	v_mul_f32_e32 v134, v133, v132
	v_fma_f32 v135, -v131, v134, v133
	v_fmac_f32_e32 v134, v135, v132
	v_fma_f32 v131, -v131, v134, v133
	v_div_fmas_f32 v131, v131, v132, v134
	v_div_fixup_f32 v130, v131, v130, 1.0
	v_pk_mul_f32 v[132:133], v[130:131], v[150:151] op_sel_hi:[0,1]
	v_pk_mul_f32 v[134:135], v[130:131], v[148:149] op_sel_hi:[0,1]
	s_waitcnt vmcnt(6)
	v_pk_fma_f32 v[150:151], v[96:97], v[132:133], v[78:79]
	v_pk_mul_f32 v[132:133], v[130:131], v[146:147] op_sel_hi:[0,1]
	v_pk_fma_f32 v[148:149], v[98:99], v[134:135], v[80:81]
	v_pk_mul_f32 v[134:135], v[130:131], v[144:145] op_sel_hi:[0,1]
	s_waitcnt vmcnt(5)
	v_pk_fma_f32 v[146:147], v[92:93], v[132:133], v[74:75]
	v_pk_mul_f32 v[132:133], v[130:131], v[142:143] op_sel_hi:[0,1]
	v_pk_fma_f32 v[144:145], v[94:95], v[134:135], v[76:77]
	v_pk_mul_f32 v[134:135], v[130:131], v[140:141] op_sel_hi:[0,1]
	s_waitcnt vmcnt(4)
	v_pk_fma_f32 v[142:143], v[88:89], v[132:133], v[70:71]
	v_pk_mul_f32 v[132:133], v[130:131], v[138:139] op_sel_hi:[0,1]
	v_pk_mul_f32 v[130:131], v[130:131], v[136:137] op_sel_hi:[0,1]
	v_pk_fma_f32 v[136:137], v[86:87], v[130:131], v[60:61]
	v_max_f32_e64 v130, |v148|, |v149|
	v_max_f32_e64 v131, |v144|, |v145|
	v_pk_fma_f32 v[140:141], v[90:91], v[134:135], v[72:73]
	v_max3_f32 v130, |v150|, |v151|, v130
	v_max3_f32 v131, |v146|, |v147|, v131
	v_pk_fma_f32 v[138:139], v[84:85], v[132:133], v[58:59]
	v_max3_f32 v130, v130, 0, v131
	v_max_f32_e64 v131, |v140|, |v141|
	v_max_f32_e64 v132, |v136|, |v137|
	v_max3_f32 v131, |v142|, |v143|, v131
	v_max3_f32 v132, |v138|, |v139|, v132
	v_max3_f32 v130, v130, v131, v132
	s_nop 1
	v_mov_b32_dpp v131, v130 quad_perm:[1,0,3,2] row_mask:0xf bank_mask:0xf bound_ctrl:1
	s_nop 0
	v_max_f32_e32 v130, v130, v131
	s_nop 1
	v_mov_b32_dpp v131, v130 quad_perm:[2,3,0,1] row_mask:0xf bank_mask:0xf bound_ctrl:1
	s_nop 0
	v_max_f32_e32 v130, v130, v131
	s_nop 1
	v_mov_b32_dpp v131, v130 row_half_mirror row_mask:0xf bank_mask:0xf bound_ctrl:1
	s_nop 0
	v_max_f32_e32 v130, v130, v131
	s_nop 1
	v_mov_b32_dpp v131, v130 row_mirror row_mask:0xf bank_mask:0xf bound_ctrl:1
	s_nop 0
	v_max_f32_e32 v130, v130, v131
	v_mov_b32_e32 v131, v130
	s_nop 1
	v_permlane16_swap_b32_e32 v130, v131
	s_nop 0
	s_nop 0
	v_max_f32_e32 v130, v130, v131
	v_mov_b32_e32 v131, v130
	s_nop 1
	v_permlane32_swap_b32_e32 v130, v131
	s_nop 0
	s_nop 0
	v_max_f32_e32 v156, v130, v131
	global_load_dwordx2 v[134:135], v[128:129], off
	global_load_dwordx2 v[132:133], v[128:129], off offset:512
	global_load_dwordx2 v[130:131], v[128:129], off offset:1024
	s_nop 0
	global_load_dwordx2 v[128:129], v[128:129], off offset:1536
	v_div_scale_f32 v162, s[0:1], v156, v156, s26
	v_rcp_f32_e32 v163, v162
	s_lshl_b64 s[0:1], s[18:19], 10
	v_fma_f32 v164, -v162, v163, 1.0
	v_fmac_f32_e32 v163, v164, v163
	v_div_scale_f32 v164, vcc, s26, v156, s26
	v_mul_f32_e32 v165, v164, v163
	v_fma_f32 v166, -v162, v165, v164
	v_fmac_f32_e32 v165, v166, v163
	v_fma_f32 v162, -v162, v165, v164
	v_div_fmas_f32 v162, v162, v163, v165
	v_div_fixup_f32 v162, v162, v156, s26
	v_cmp_lt_f32_e32 vcc, 0, v156
	s_nop 1
	v_cndmask_b32_e32 v164, 0, v162, vcc
	v_mul_f32_e32 v166, v164, v151
	v_mul_f32_e32 v165, v164, v150
	v_rndne_f32_e32 v166, v166
	v_mul_f32_e32 v167, v164, v148
	v_mul_f32_e32 v168, v164, v149
	v_rndne_f32_e32 v165, v165
	v_rndne_f32_e32 v167, v167
	v_rndne_f32_e32 v168, v168
	v_cvt_i32_f32_e32 v166, v166
	v_cvt_i32_f32_e32 v165, v165
	v_cvt_i32_f32_sdwa v167, v167 dst_sel:WORD_1 dst_unused:UNUSED_PAD src0_sel:DWORD
	v_cvt_i32_f32_e32 v168, v168
	v_lshlrev_b32_e32 v166, 8, v166
	v_and_b32_e32 v166, 0xff00, v166
	v_and_b32_e32 v167, 0xff0000, v167
	v_perm_b32 v165, v168, v165, s27
	v_lshl_add_u64 v[162:163], v[118:119], 0, s[0:1]
	v_or3_b32 v165, v165, v166, v167
	v_mul_f32_e32 v166, v164, v147
	global_store_dword v[162:163], v165, off
	v_mul_f32_e32 v165, v164, v146
	v_rndne_f32_e32 v166, v166
	v_mul_f32_e32 v167, v164, v144
	v_mul_f32_e32 v168, v164, v145
	v_rndne_f32_e32 v165, v165
	v_rndne_f32_e32 v167, v167
	v_rndne_f32_e32 v168, v168
	v_cvt_i32_f32_e32 v166, v166
	v_cvt_i32_f32_e32 v165, v165
	v_cvt_i32_f32_sdwa v167, v167 dst_sel:WORD_1 dst_unused:UNUSED_PAD src0_sel:DWORD
	v_cvt_i32_f32_e32 v168, v168
	v_lshlrev_b32_e32 v166, 8, v166
	v_and_b32_e32 v166, 0xff00, v166
	v_and_b32_e32 v167, 0xff0000, v167
	v_perm_b32 v165, v168, v165, s27
	v_or3_b32 v165, v165, v166, v167
	v_mul_f32_e32 v166, v164, v143
	global_store_dword v[162:163], v165, off offset:256
	v_mul_f32_e32 v165, v164, v142
	v_rndne_f32_e32 v166, v166
	v_mul_f32_e32 v167, v164, v140
	v_mul_f32_e32 v168, v164, v141
	v_rndne_f32_e32 v165, v165
	v_rndne_f32_e32 v167, v167
	v_rndne_f32_e32 v168, v168
	v_cvt_i32_f32_e32 v166, v166
	v_cvt_i32_f32_e32 v165, v165
	v_cvt_i32_f32_sdwa v167, v167 dst_sel:WORD_1 dst_unused:UNUSED_PAD src0_sel:DWORD
	v_cvt_i32_f32_e32 v168, v168
	v_lshlrev_b32_e32 v166, 8, v166
	v_and_b32_e32 v166, 0xff00, v166
	v_and_b32_e32 v167, 0xff0000, v167
	v_perm_b32 v165, v168, v165, s27
	v_or3_b32 v165, v165, v166, v167
	v_mul_f32_e32 v166, v164, v139
	global_store_dword v[162:163], v165, off offset:512
	v_mul_f32_e32 v165, v164, v138
	v_rndne_f32_e32 v166, v166
	v_mul_f32_e32 v167, v164, v136
	v_mul_f32_e32 v164, v164, v137
	v_rndne_f32_e32 v165, v165
	v_rndne_f32_e32 v167, v167
	v_rndne_f32_e32 v164, v164
	v_cvt_i32_f32_e32 v166, v166
	v_cvt_i32_f32_e32 v165, v165
	v_cvt_i32_f32_sdwa v167, v167 dst_sel:WORD_1 dst_unused:UNUSED_PAD src0_sel:DWORD
	v_cvt_i32_f32_e32 v164, v164
	v_lshlrev_b32_e32 v166, 8, v166
	v_and_b32_e32 v166, 0xff00, v166
	v_and_b32_e32 v167, 0xff0000, v167
	v_perm_b32 v164, v164, v165, s27
	v_or3_b32 v164, v164, v166, v167
	global_store_dword v[162:163], v164, off offset:768
	s_and_saveexec_b64 s[0:1], s[14:15]
	s_cbranch_execz .LBB0_2989
	s_add_i32 s28, s24, 0
	s_add_i32 s30, s28, 0x23500
	s_lshl_b64 s[28:29], s[18:19], 2
	s_add_u32 s28, s82, s28
	s_addc_u32 s29, s83, s29
	v_mul_f32_e32 v156, 0x3c010204, v156
	v_mov_b32_e32 v162, s30
	global_store_dword v83, v156, s[28:29]
	ds_write_b32 v162, v156
.LBB0_2989:
	s_or_b64 exec, exec, s[0:1]
	v_cvt_pk_bf16_f32 v162, v150, v151
	v_cvt_pk_bf16_f32 v163, v148, v149
	v_lshlrev_b32_e32 v164, 16, v162
	v_and_b32_e32 v165, 0xffff0000, v162
	v_pk_add_f32 v[150:151], v[150:151], v[164:165] neg_lo:[0,1] neg_hi:[0,1]
	v_lshlrev_b32_e32 v164, 16, v163
	v_and_b32_e32 v165, 0xffff0000, v163
	v_pk_add_f32 v[148:149], v[148:149], v[164:165] neg_lo:[0,1] neg_hi:[0,1]
	v_add_u32_e32 v156, 0, v158
	v_cvt_pk_bf16_f32 v150, v150, v151
	v_cvt_pk_bf16_f32 v151, v148, v149
	v_cvt_pk_bf16_f32 v148, v146, v147
	v_cvt_pk_bf16_f32 v149, v144, v145
	ds_write2st64_b64 v156, v[162:163], v[148:149] offset1:1
	v_lshlrev_b32_e32 v162, 16, v148
	v_and_b32_e32 v163, 0xffff0000, v148
	v_lshlrev_b32_e32 v148, 16, v149
	v_and_b32_e32 v149, 0xffff0000, v149
	v_pk_add_f32 v[146:147], v[146:147], v[162:163] neg_lo:[0,1] neg_hi:[0,1]
	v_pk_add_f32 v[144:145], v[144:145], v[148:149] neg_lo:[0,1] neg_hi:[0,1]
	v_cvt_pk_bf16_f32 v146, v146, v147
	v_cvt_pk_bf16_f32 v147, v144, v145
	v_add_u32_e32 v148, 0x100, v156
	v_cvt_pk_bf16_f32 v144, v142, v143
	ds_write2st64_b64 v148, v[150:151], v[146:147] offset0:64 offset1:65
	v_cvt_pk_bf16_f32 v145, v140, v141
	v_lshlrev_b32_e32 v146, 16, v144
	v_and_b32_e32 v147, 0xffff0000, v144
	v_pk_add_f32 v[142:143], v[142:143], v[146:147] neg_lo:[0,1] neg_hi:[0,1]
	v_lshlrev_b32_e32 v146, 16, v145
	v_and_b32_e32 v147, 0xffff0000, v145
	v_pk_add_f32 v[140:141], v[140:141], v[146:147] neg_lo:[0,1] neg_hi:[0,1]
	v_cvt_pk_bf16_f32 v142, v142, v143
	v_cvt_pk_bf16_f32 v143, v140, v141
	v_cvt_pk_bf16_f32 v140, v138, v139
	v_cvt_pk_bf16_f32 v141, v136, v137
	ds_write2st64_b64 v156, v[144:145], v[140:141] offset0:2 offset1:3
	v_lshlrev_b32_e32 v144, 16, v140
	v_and_b32_e32 v145, 0xffff0000, v140
	v_pk_add_f32 v[138:139], v[138:139], v[144:145] neg_lo:[0,1] neg_hi:[0,1]
	v_mul_f32_e32 v140, v115, v115
	v_mul_f32_e32 v144, v113, v113
	v_fmac_f32_e32 v140, v114, v114
	v_fmac_f32_e32 v144, v112, v112
	v_add_f32_e32 v140, v140, v144
	v_mul_f32_e32 v144, v111, v111
	v_mul_f32_e32 v145, v109, v109
	v_fmac_f32_e32 v144, v110, v110
	v_fmac_f32_e32 v145, v108, v108
	v_add_f32_e32 v144, v144, v145
	v_add_f32_e32 v140, v144, v140
	v_mul_f32_e32 v144, v107, v107
	v_mul_f32_e32 v145, v105, v105
	v_fmac_f32_e32 v144, v106, v106
	v_fmac_f32_e32 v145, v104, v104
	v_add_f32_e32 v144, v144, v145
	v_add_f32_e32 v140, v144, v140
	v_mul_f32_e32 v144, v103, v103
	v_mul_f32_e32 v145, v101, v101
	v_fmac_f32_e32 v144, v102, v102
	v_fmac_f32_e32 v145, v100, v100
	v_add_f32_e32 v144, v144, v145
	v_add_f32_e32 v140, v144, v140
	v_cvt_pk_bf16_f32 v138, v138, v139
	s_nop 0
	v_add_f32_dpp v140, v140, v140 quad_perm:[1,0,3,2] row_mask:0xf bank_mask:0xf bound_ctrl:1
	s_nop 1
	v_add_f32_dpp v140, v140, v140 quad_perm:[2,3,0,1] row_mask:0xf bank_mask:0xf bound_ctrl:1
	s_nop 1
	v_add_f32_dpp v140, v140, v140 row_half_mirror row_mask:0xf bank_mask:0xf bound_ctrl:1
	s_nop 1
	v_add_f32_dpp v140, v140, v140 row_mirror row_mask:0xf bank_mask:0xf bound_ctrl:1
	v_mov_b32_e32 v144, v140
	s_nop 1
	v_permlane16_swap_b32_e32 v140, v144
	v_add_f32_e32 v140, v140, v144
	v_mov_b32_e32 v144, v140
	s_nop 1
	v_permlane32_swap_b32_e32 v140, v144
	v_add_f32_e32 v140, v140, v144
	v_fmamk_f32 v140, v140, 0x3a800000, v159
	v_mul_f32_e32 v144, 0x4f800000, v140
	v_cmp_gt_f32_e32 vcc, s25, v140
	s_nop 1
	v_cndmask_b32_e32 v144, v140, v144, vcc
	v_sqrt_f32_e32 v145, v144
	v_lshlrev_b32_e32 v140, 16, v141
	v_and_b32_e32 v141, 0xffff0000, v141
	v_pk_add_f32 v[136:137], v[136:137], v[140:141] neg_lo:[0,1] neg_hi:[0,1]
	v_add_u32_e32 v139, -1, v145
	v_fma_f32 v146, -v139, v145, v144
	v_cmp_ge_f32_e64 s[0:1], 0, v146
	v_add_u32_e32 v146, 1, v145
	s_nop 0
	v_cndmask_b32_e64 v139, v145, v139, s[0:1]
	v_fma_f32 v145, -v146, v145, v144
	v_cmp_lt_f32_e64 s[0:1], 0, v145
	s_nop 1
	v_cndmask_b32_e64 v139, v139, v146, s[0:1]
	v_mul_f32_e32 v145, 0x37800000, v139
	v_cndmask_b32_e32 v139, v139, v145, vcc
	v_cmp_class_f32_e32 vcc, v144, v160
	s_nop 1
	v_cndmask_b32_e32 v144, v139, v144, vcc
	v_div_scale_f32 v145, s[0:1], v144, v144, 1.0
	v_rcp_f32_e32 v146, v145
	v_cvt_pk_bf16_f32 v139, v136, v137
	ds_write2st64_b64 v148, v[142:143], v[138:139] offset0:66 offset1:67
	v_fma_f32 v136, -v145, v146, 1.0
	v_fmac_f32_e32 v146, v136, v146
	v_div_scale_f32 v136, vcc, 1.0, v144, 1.0
	v_mul_f32_e32 v137, v136, v146
	v_fma_f32 v138, -v145, v137, v136
	v_fmac_f32_e32 v137, v138, v146
	v_fma_f32 v136, -v145, v137, v136
	v_div_fmas_f32 v136, v136, v146, v137
	v_div_fixup_f32 v136, v136, v144, 1.0
	v_pk_mul_f32 v[112:113], v[136:137], v[112:113] op_sel_hi:[0,1]
	v_pk_mul_f32 v[108:109], v[136:137], v[108:109] op_sel_hi:[0,1]
	v_pk_mul_f32 v[114:115], v[136:137], v[114:115] op_sel_hi:[0,1]
	v_pk_fma_f32 v[112:113], v[98:99], v[112:113], v[80:81]
	v_pk_mul_f32 v[110:111], v[136:137], v[110:111] op_sel_hi:[0,1]
	v_pk_fma_f32 v[108:109], v[94:95], v[108:109], v[76:77]
	v_pk_fma_f32 v[114:115], v[96:97], v[114:115], v[78:79]
	v_pk_fma_f32 v[110:111], v[92:93], v[110:111], v[74:75]
	v_pk_mul_f32 v[106:107], v[136:137], v[106:107] op_sel_hi:[0,1]
	v_pk_mul_f32 v[104:105], v[136:137], v[104:105] op_sel_hi:[0,1]
	v_pk_mul_f32 v[102:103], v[136:137], v[102:103] op_sel_hi:[0,1]
	v_pk_mul_f32 v[100:101], v[136:137], v[100:101] op_sel_hi:[0,1]
	v_max_f32_e64 v136, |v112|, |v113|
	v_max_f32_e64 v137, |v108|, |v109|
	v_pk_fma_f32 v[104:105], v[90:91], v[104:105], v[72:73]
	v_pk_fma_f32 v[100:101], v[86:87], v[100:101], v[60:61]
	v_max3_f32 v136, |v114|, |v115|, v136
	v_max3_f32 v137, |v110|, |v111|, v137
	v_pk_fma_f32 v[106:107], v[88:89], v[106:107], v[70:71]
	v_pk_fma_f32 v[102:103], v[84:85], v[102:103], v[58:59]
	v_max3_f32 v136, v136, 0, v137
	v_max_f32_e64 v137, |v104|, |v105|
	v_max_f32_e64 v138, |v100|, |v101|
	v_max3_f32 v137, |v106|, |v107|, v137
	v_max3_f32 v138, |v102|, |v103|, v138
	v_max3_f32 v136, v136, v137, v138
	s_nop 1
	v_mov_b32_dpp v137, v136 quad_perm:[1,0,3,2] row_mask:0xf bank_mask:0xf bound_ctrl:1
	s_nop 0
	v_max_f32_e32 v136, v136, v137
	s_nop 1
	v_mov_b32_dpp v137, v136 quad_perm:[2,3,0,1] row_mask:0xf bank_mask:0xf bound_ctrl:1
	s_nop 0
	v_max_f32_e32 v136, v136, v137
	s_nop 1
	v_mov_b32_dpp v137, v136 row_half_mirror row_mask:0xf bank_mask:0xf bound_ctrl:1
	s_nop 0
	v_max_f32_e32 v136, v136, v137
	s_nop 1
	v_mov_b32_dpp v137, v136 row_mirror row_mask:0xf bank_mask:0xf bound_ctrl:1
	s_nop 0
	v_max_f32_e32 v136, v136, v137
	v_mov_b32_e32 v137, v136
	s_nop 1
	v_permlane16_swap_b32_e32 v136, v137
	s_nop 0
	s_nop 0
	v_max_f32_e32 v136, v136, v137
	v_mov_b32_e32 v137, v136
	s_nop 1
	v_permlane32_swap_b32_e32 v136, v137
	s_nop 0
	s_nop 0
	v_max_f32_e32 v136, v136, v137
	v_div_scale_f32 v137, s[0:1], v136, v136, s26
	v_rcp_f32_e32 v138, v137
	s_add_i32 s0, s18, 1
	s_ashr_i32 s1, s0, 31
	s_lshl_b64 s[18:19], s[0:1], 10
	v_fma_f32 v139, -v137, v138, 1.0
	v_fmac_f32_e32 v138, v139, v138
	v_div_scale_f32 v139, vcc, s26, v136, s26
	v_mul_f32_e32 v140, v139, v138
	v_fma_f32 v141, -v137, v140, v139
	v_fmac_f32_e32 v140, v141, v138
	v_fma_f32 v137, -v137, v140, v139
	v_div_fmas_f32 v137, v137, v138, v140
	v_div_fixup_f32 v137, v137, v136, s26
	v_cmp_lt_f32_e32 vcc, 0, v136
	v_lshl_add_u64 v[138:139], v[118:119], 0, s[18:19]
	s_nop 0
	v_cndmask_b32_e32 v137, 0, v137, vcc
	v_mul_f32_e32 v141, v137, v115
	v_mul_f32_e32 v140, v137, v114
	v_rndne_f32_e32 v141, v141
	v_mul_f32_e32 v142, v137, v112
	v_mul_f32_e32 v143, v137, v113
	v_rndne_f32_e32 v140, v140
	v_rndne_f32_e32 v142, v142
	v_rndne_f32_e32 v143, v143
	v_cvt_i32_f32_e32 v141, v141
	v_cvt_i32_f32_e32 v140, v140
	v_cvt_i32_f32_sdwa v142, v142 dst_sel:WORD_1 dst_unused:UNUSED_PAD src0_sel:DWORD
	v_cvt_i32_f32_e32 v143, v143
	v_lshlrev_b32_e32 v141, 8, v141
	v_and_b32_e32 v141, 0xff00, v141
	v_and_b32_e32 v142, 0xff0000, v142
	v_perm_b32 v140, v143, v140, s27
	v_or3_b32 v140, v140, v141, v142
	v_mul_f32_e32 v141, v137, v111
	global_store_dword v[138:139], v140, off
	v_mul_f32_e32 v140, v137, v110
	v_rndne_f32_e32 v141, v141
	v_mul_f32_e32 v142, v137, v108
	v_mul_f32_e32 v143, v137, v109
	v_rndne_f32_e32 v140, v140
	v_rndne_f32_e32 v142, v142
	v_rndne_f32_e32 v143, v143
	v_cvt_i32_f32_e32 v141, v141
	v_cvt_i32_f32_e32 v140, v140
	v_cvt_i32_f32_sdwa v142, v142 dst_sel:WORD_1 dst_unused:UNUSED_PAD src0_sel:DWORD
	v_cvt_i32_f32_e32 v143, v143
	v_lshlrev_b32_e32 v141, 8, v141
	v_and_b32_e32 v141, 0xff00, v141
	v_and_b32_e32 v142, 0xff0000, v142
	v_perm_b32 v140, v143, v140, s27
	v_or3_b32 v140, v140, v141, v142
	v_mul_f32_e32 v141, v137, v107
	global_store_dword v[138:139], v140, off offset:256
	v_mul_f32_e32 v140, v137, v106
	v_rndne_f32_e32 v141, v141
	v_mul_f32_e32 v142, v137, v104
	v_mul_f32_e32 v143, v137, v105
	v_rndne_f32_e32 v140, v140
	v_rndne_f32_e32 v142, v142
	v_rndne_f32_e32 v143, v143
	v_cvt_i32_f32_e32 v141, v141
	v_cvt_i32_f32_e32 v140, v140
	v_cvt_i32_f32_sdwa v142, v142 dst_sel:WORD_1 dst_unused:UNUSED_PAD src0_sel:DWORD
	v_cvt_i32_f32_e32 v143, v143
	v_lshlrev_b32_e32 v141, 8, v141
	v_and_b32_e32 v141, 0xff00, v141
	v_and_b32_e32 v142, 0xff0000, v142
	v_perm_b32 v140, v143, v140, s27
	v_or3_b32 v140, v140, v141, v142
	v_mul_f32_e32 v141, v137, v103
	global_store_dword v[138:139], v140, off offset:512
	v_mul_f32_e32 v140, v137, v102
	v_rndne_f32_e32 v141, v141
	v_mul_f32_e32 v142, v137, v100
	v_mul_f32_e32 v137, v137, v101
	v_rndne_f32_e32 v140, v140
	v_rndne_f32_e32 v142, v142
	v_rndne_f32_e32 v137, v137
	v_cvt_i32_f32_e32 v141, v141
	v_cvt_i32_f32_e32 v140, v140
	v_cvt_i32_f32_sdwa v142, v142 dst_sel:WORD_1 dst_unused:UNUSED_PAD src0_sel:DWORD
	v_cvt_i32_f32_e32 v137, v137
	v_lshlrev_b32_e32 v141, 8, v141
	v_and_b32_e32 v141, 0xff00, v141
	v_and_b32_e32 v142, 0xff0000, v142
	v_perm_b32 v137, v137, v140, s27
	v_or3_b32 v137, v137, v141, v142
	global_store_dword v[138:139], v137, off offset:768
	s_and_saveexec_b64 s[18:19], s[14:15]
	s_cbranch_execz .LBB0_2991
	s_add_i32 s28, s24, 0
	s_add_i32 s28, s28, 0x23504
	s_lshl_b64 s[0:1], s[0:1], 2
	s_add_u32 s0, s82, s0
	s_addc_u32 s1, s83, s1
	v_mul_f32_e32 v136, 0x3c010204, v136
	v_mov_b32_e32 v137, s28
	global_store_dword v83, v136, s[0:1]
	ds_write_b32 v137, v136
.LBB0_2991:
	s_or_b64 exec, exec, s[18:19]
	v_cvt_pk_bf16_f32 v136, v114, v115
	v_cvt_pk_bf16_f32 v137, v112, v113
	v_lshlrev_b32_e32 v138, 16, v136
	v_and_b32_e32 v139, 0xffff0000, v136
	v_pk_add_f32 v[114:115], v[114:115], v[138:139] neg_lo:[0,1] neg_hi:[0,1]
	v_lshlrev_b32_e32 v138, 16, v137
	v_and_b32_e32 v139, 0xffff0000, v137
	v_pk_add_f32 v[112:113], v[112:113], v[138:139] neg_lo:[0,1] neg_hi:[0,1]
	v_cvt_pk_bf16_f32 v114, v114, v115
	v_cvt_pk_bf16_f32 v115, v112, v113
	v_cvt_pk_bf16_f32 v112, v110, v111
	v_cvt_pk_bf16_f32 v113, v108, v109
	v_add_u32_e32 v138, 16, v156
	ds_write2st64_b64 v138, v[136:137], v[112:113] offset0:4 offset1:5
	v_lshlrev_b32_e32 v136, 16, v112
	v_and_b32_e32 v137, 0xffff0000, v112
	v_lshlrev_b32_e32 v112, 16, v113
	v_and_b32_e32 v113, 0xffff0000, v113
	v_pk_add_f32 v[110:111], v[110:111], v[136:137] neg_lo:[0,1] neg_hi:[0,1]
	v_pk_add_f32 v[108:109], v[108:109], v[112:113] neg_lo:[0,1] neg_hi:[0,1]
	v_cvt_pk_bf16_f32 v110, v110, v111
	v_cvt_pk_bf16_f32 v111, v108, v109
	v_add_u32_e32 v112, 0x110, v156
	v_cvt_pk_bf16_f32 v108, v106, v107
	ds_write2st64_b64 v112, v[114:115], v[110:111] offset0:68 offset1:69
	v_cvt_pk_bf16_f32 v109, v104, v105
	v_lshlrev_b32_e32 v110, 16, v108
	v_and_b32_e32 v111, 0xffff0000, v108
	v_pk_add_f32 v[106:107], v[106:107], v[110:111] neg_lo:[0,1] neg_hi:[0,1]
	v_lshlrev_b32_e32 v110, 16, v109
	v_and_b32_e32 v111, 0xffff0000, v109
	v_pk_add_f32 v[104:105], v[104:105], v[110:111] neg_lo:[0,1] neg_hi:[0,1]
	v_cvt_pk_bf16_f32 v106, v106, v107
	v_cvt_pk_bf16_f32 v107, v104, v105
	v_cvt_pk_bf16_f32 v104, v102, v103
	v_cvt_pk_bf16_f32 v105, v100, v101
	ds_write2st64_b64 v138, v[108:109], v[104:105] offset0:6 offset1:7
	v_lshlrev_b32_e32 v108, 16, v104
	v_and_b32_e32 v109, 0xffff0000, v104
	v_lshlrev_b32_e32 v104, 16, v105
	v_and_b32_e32 v105, 0xffff0000, v105
	v_pk_add_f32 v[102:103], v[102:103], v[108:109] neg_lo:[0,1] neg_hi:[0,1]
	v_pk_add_f32 v[100:101], v[100:101], v[104:105] neg_lo:[0,1] neg_hi:[0,1]
	v_cvt_pk_bf16_f32 v102, v102, v103
	v_cvt_pk_bf16_f32 v103, v100, v101
	v_add_u32_e32 v162, 0, v157
	ds_write2st64_b64 v112, v[106:107], v[102:103] offset0:70 offset1:71
	s_waitcnt lgkmcnt(0)
	s_barrier
	ds_read_b128 v[100:103], v162
	ds_read_b128 v[104:107], v162 offset:64
	s_waitcnt lgkmcnt(1)
	v_mfma_f32_16x16x32_bf16 v[108:111], v[100:103], v[2:5], 0
	ds_read_b128 v[136:139], v162 offset:33024
	ds_read_b128 v[140:143], v162 offset:33088
	v_mfma_f32_16x16x32_bf16 v[112:115], v[100:103], v[6:9], 0
	s_waitcnt lgkmcnt(1)
	v_mfma_f32_16x16x32_bf16 v[108:111], v[136:139], v[2:5], v[108:111]
	v_mfma_f32_16x16x32_bf16 v[112:115], v[136:139], v[6:9], v[112:115]
	v_mfma_f32_16x16x32_bf16 v[108:111], v[100:103], v[10:13], v[108:111]
	v_mfma_f32_16x16x32_bf16 v[100:103], v[100:103], v[14:17], v[112:115]
	v_mfma_f32_16x16x32_bf16 v[108:111], v[104:107], v[18:21], v[108:111]
	v_mfma_f32_16x16x32_bf16 v[100:103], v[104:107], v[22:25], v[100:103]
	s_waitcnt lgkmcnt(0)
	v_mfma_f32_16x16x32_bf16 v[108:111], v[140:143], v[18:21], v[108:111]
	v_mfma_f32_16x16x32_bf16 v[100:103], v[140:143], v[22:25], v[100:103]
	v_mfma_f32_16x16x32_bf16 v[108:111], v[104:107], v[26:29], v[108:111]
	v_mfma_f32_16x16x32_bf16 v[100:103], v[104:107], v[34:37], v[100:103]
	ds_read_b128 v[104:107], v162 offset:128
	ds_read_b128 v[112:115], v162 offset:192
	ds_read_b128 v[136:139], v162 offset:33152
	ds_read_b128 v[140:143], v162 offset:33216
	s_waitcnt lgkmcnt(3)
	v_mfma_f32_16x16x32_bf16 v[108:111], v[104:107], v[30:33], v[108:111]
	v_mfma_f32_16x16x32_bf16 v[100:103], v[104:107], v[38:41], v[100:103]
	s_waitcnt lgkmcnt(1)
	v_mfma_f32_16x16x32_bf16 v[108:111], v[136:139], v[30:33], v[108:111]
	v_mfma_f32_16x16x32_bf16 v[100:103], v[136:139], v[38:41], v[100:103]
	v_mfma_f32_16x16x32_bf16 v[108:111], v[104:107], v[42:45], v[108:111]
	v_mfma_f32_16x16x32_bf16 v[100:103], v[104:107], v[46:49], v[100:103]
	v_mfma_f32_16x16x32_bf16 v[104:107], v[112:115], v[50:53], v[108:111]
	v_mfma_f32_16x16x32_bf16 v[100:103], v[112:115], v[54:57], v[100:103]
	s_waitcnt lgkmcnt(0)
	v_mfma_f32_16x16x32_bf16 v[104:107], v[140:143], v[50:53], v[104:107]
	v_mfma_f32_16x16x32_bf16 v[100:103], v[140:143], v[54:57], v[100:103]
	v_mfma_f32_16x16x32_bf16 v[104:107], v[112:115], v[62:65], v[104:107]
	v_mfma_f32_16x16x32_bf16 v[100:103], v[112:115], v[66:69], v[100:103]
	s_nop 7
	ds_write2_b32 v155, v104, v100 offset1:16
	ds_write2_b32 v155, v105, v101 offset0:32 offset1:48
	ds_write2_b32 v155, v106, v102 offset0:64 offset1:80
	ds_write2_b32 v155, v107, v103 offset0:96 offset1:112
	s_waitcnt lgkmcnt(0)
	s_barrier
	ds_read2st64_b32 v[100:101], v154 offset1:8
	ds_read2st64_b32 v[102:103], v154 offset0:16 offset1:24
	ds_read2st64_b32 v[104:105], v154 offset0:32 offset1:40
	s_waitcnt lgkmcnt(2)
	v_add_f32_e32 v100, v1, v100
	v_add_f32_e32 v106, v100, v101
	ds_read2st64_b32 v[100:101], v154 offset0:48 offset1:56
	s_waitcnt lgkmcnt(2)
	v_add_f32_e32 v102, v106, v102
	v_add_f32_e32 v102, v102, v103
	s_waitcnt lgkmcnt(1)
	v_add_f32_e32 v102, v102, v104
	v_add_f32_e32 v102, v102, v105
	s_waitcnt lgkmcnt(0)
	v_add_f32_e32 v100, v102, v100
	v_add_f32_e32 v102, v100, v101
	s_nop 1
	v_mov_b32_dpp v100, v102 quad_perm:[1,0,3,2] row_mask:0xf bank_mask:0xf bound_ctrl:1
	s_nop 0
	v_max_f32_e32 v100, v102, v100
	s_nop 1
	v_mov_b32_dpp v101, v100 quad_perm:[2,3,0,1] row_mask:0xf bank_mask:0xf bound_ctrl:1
	s_nop 0
	v_max_f32_e32 v100, v100, v101
	s_nop 1
	v_mov_b32_dpp v101, v100 row_half_mirror row_mask:0xf bank_mask:0xf bound_ctrl:1
	s_nop 0
	v_max_f32_e32 v100, v100, v101
	s_nop 1
	v_mov_b32_dpp v101, v100 row_mirror row_mask:0xf bank_mask:0xf bound_ctrl:1
	s_nop 0
	v_max_f32_e32 v100, v100, v101
	v_mov_b32_e32 v101, v100
	s_nop 1
	v_permlane16_swap_b32_e32 v100, v101
	s_nop 0
	s_nop 0
	v_max_f32_e32 v101, v100, v101
	v_cmp_eq_f32_e32 vcc, v102, v101
	s_nop 1
	v_mov_b32_e32 v100, vcc_hi
	v_mov_b32_e32 v103, vcc_lo
	v_cndmask_b32_e64 v100, v100, v103, s[10:11]
	v_ffbl_b32_e32 v100, v100
	v_cmp_ne_u32_e32 vcc, v178, v100
	s_nop 1
	v_cndmask_b32_e32 v103, v161, v102, vcc
	s_nop 1
	v_mov_b32_dpp v102, v103 quad_perm:[1,0,3,2] row_mask:0xf bank_mask:0xf bound_ctrl:1
	s_nop 0
	v_max_f32_e32 v102, v103, v102
	s_nop 1
	v_mov_b32_dpp v104, v102 quad_perm:[2,3,0,1] row_mask:0xf bank_mask:0xf bound_ctrl:1
	s_nop 0
	v_max_f32_e32 v102, v102, v104
	s_nop 1
	v_mov_b32_dpp v104, v102 row_half_mirror row_mask:0xf bank_mask:0xf bound_ctrl:1
	s_nop 0
	v_max_f32_e32 v102, v102, v104
	s_nop 1
	v_mov_b32_dpp v104, v102 row_mirror row_mask:0xf bank_mask:0xf bound_ctrl:1
	s_nop 0
	v_max_f32_e32 v102, v102, v104
	v_mov_b32_e32 v104, v102
	s_nop 1
	v_permlane16_swap_b32_e32 v102, v104
	s_nop 0
	s_nop 0
	v_max_f32_e32 v104, v102, v104
	v_cmp_eq_f32_e32 vcc, v103, v104
	s_nop 1
	v_mov_b32_e32 v102, vcc_hi
	v_mov_b32_e32 v105, vcc_lo
	v_cndmask_b32_e64 v102, v102, v105, s[10:11]
	v_ffbl_b32_e32 v102, v102
	v_cmp_ne_u32_e32 vcc, v178, v102
	s_nop 1
	v_cndmask_b32_e32 v106, v161, v103, vcc
	s_nop 1
	v_mov_b32_dpp v103, v106 quad_perm:[1,0,3,2] row_mask:0xf bank_mask:0xf bound_ctrl:1
	s_nop 0
	v_max_f32_e32 v103, v106, v103
	s_nop 1
	v_mov_b32_dpp v105, v103 quad_perm:[2,3,0,1] row_mask:0xf bank_mask:0xf bound_ctrl:1
	s_nop 0
	v_max_f32_e32 v103, v103, v105
	s_nop 1
	v_mov_b32_dpp v105, v103 row_half_mirror row_mask:0xf bank_mask:0xf bound_ctrl:1
	s_nop 0
	v_max_f32_e32 v103, v103, v105
	s_nop 1
	v_mov_b32_dpp v105, v103 row_mirror row_mask:0xf bank_mask:0xf bound_ctrl:1
	s_nop 0
	v_max_f32_e32 v103, v103, v105
	v_mov_b32_e32 v105, v103
	s_nop 1
	v_permlane16_swap_b32_e32 v103, v105
	s_nop 0
	s_nop 0
	v_max_f32_e32 v105, v103, v105
	v_cmp_eq_f32_e32 vcc, v106, v105
	s_nop 1
	v_mov_b32_e32 v103, vcc_hi
	v_mov_b32_e32 v107, vcc_lo
	v_cndmask_b32_e64 v103, v103, v107, s[10:11]
	v_ffbl_b32_e32 v103, v103
	v_cmp_ne_u32_e32 vcc, v178, v103
	s_nop 1
	v_cndmask_b32_e32 v107, v161, v106, vcc
	s_nop 1
	v_mov_b32_dpp v106, v107 quad_perm:[1,0,3,2] row_mask:0xf bank_mask:0xf bound_ctrl:1
	s_nop 0
	v_max_f32_e32 v106, v107, v106
	s_nop 1
	v_mov_b32_dpp v108, v106 quad_perm:[2,3,0,1] row_mask:0xf bank_mask:0xf bound_ctrl:1
	s_nop 0
	v_max_f32_e32 v106, v106, v108
	s_nop 1
	v_mov_b32_dpp v108, v106 row_half_mirror row_mask:0xf bank_mask:0xf bound_ctrl:1
	s_nop 0
	v_max_f32_e32 v106, v106, v108
	s_nop 1
	v_mov_b32_dpp v108, v106 row_mirror row_mask:0xf bank_mask:0xf bound_ctrl:1
	s_nop 0
	v_max_f32_e32 v106, v106, v108
	v_mov_b32_e32 v108, v106
	s_nop 1
	v_permlane16_swap_b32_e32 v106, v108
	s_nop 0
	s_nop 0
	v_max_f32_e32 v106, v106, v108
	v_cmp_eq_f32_e64 s[0:1], v107, v106
	s_and_saveexec_b64 s[18:19], s[12:13]
	s_cbranch_execz .LBB0_2986
	v_sub_f32_e32 v104, v104, v101
	v_mul_f32_e32 v104, 0x3fb8aa3b, v104
	v_sub_f32_e32 v105, v105, v101
	v_exp_f32_e32 v104, v104
	v_mul_f32_e32 v105, 0x3fb8aa3b, v105
	v_sub_f32_e32 v101, v106, v101
	v_exp_f32_e32 v105, v105
	v_mul_f32_e32 v101, 0x3fb8aa3b, v101
	v_exp_f32_e32 v101, v101
	v_add_f32_e32 v106, 1.0, v104
	v_add_f32_e32 v106, v106, v105
	v_add_f32_e32 v106, v106, v101
	v_div_scale_f32 v107, s[28:29], v106, v106, 1.0
	v_rcp_f32_e32 v108, v107
	v_cndmask_b32_e64 v101, v101, v105, s[8:9]
	v_cndmask_b32_e64 v101, v101, v104, s[6:7]
	v_cndmask_b32_e64 v101, v101, 1.0, s[4:5]
	v_fma_f32 v109, -v107, v108, 1.0
	v_fmac_f32_e32 v108, v109, v108
	v_div_scale_f32 v109, vcc, 1.0, v106, 1.0
	v_mul_f32_e32 v110, v109, v108
	v_fma_f32 v111, -v107, v110, v109
	v_fmac_f32_e32 v110, v111, v108
	v_fma_f32 v107, -v107, v110, v109
	v_div_fmas_f32 v107, v107, v108, v110
	v_div_fixup_f32 v106, v107, v106, 1.0
	v_mov_b32_e32 v107, s1
	v_mov_b32_e32 v108, s0
	v_cndmask_b32_e64 v107, v107, v108, s[10:11]
	v_ffbl_b32_e32 v107, v107
	v_cndmask_b32_e64 v103, v107, v103, s[8:9]
	v_cndmask_b32_e64 v102, v103, v102, s[6:7]
	v_cndmask_b32_e64 v100, v102, v100, s[4:5]
	v_lshl_add_u32 v102, v100, 2, 0
	v_add_u32_e32 v102, 0x20400, v102
	ds_add_rtn_u32 v102, v102, v153
	v_add_u32_e32 v103, 0, v82
	v_add_u32_e32 v104, 0x20500, v103
	ds_write_b32 v104, v100
	v_add_u32_e32 v100, 0x21500, v103
	v_mul_f32_e32 v101, v106, v101
	s_waitcnt lgkmcnt(1)
	ds_write_b32 v100, v102
	v_add_u32_e32 v100, 0x22500, v103
	ds_write_b32 v100, v101
	s_branch .LBB0_2986
.LBB0_2993:
	v_mul_f32_e32 v82, v151, v151
	v_mul_f32_e32 v83, v149, v149
	v_fmac_f32_e32 v82, v150, v150
	v_fmac_f32_e32 v83, v148, v148
	v_add_f32_e32 v82, v82, v83
	v_mul_f32_e32 v83, v147, v147
	v_mul_f32_e32 v116, v145, v145
	v_fmac_f32_e32 v83, v146, v146
	v_fmac_f32_e32 v116, v144, v144
	v_add_f32_e32 v83, v83, v116
	v_add_f32_e32 v82, v82, v83
	v_mul_f32_e32 v83, v143, v143
	v_mul_f32_e32 v116, v141, v141
	v_fmac_f32_e32 v83, v142, v142
	v_fmac_f32_e32 v116, v140, v140
	v_add_f32_e32 v83, v83, v116
	v_add_f32_e32 v82, v83, v82
	v_mul_f32_e32 v83, v139, v139
	v_mul_f32_e32 v116, v137, v137
	v_fmac_f32_e32 v83, v138, v138
	v_fmac_f32_e32 v116, v136, v136
	v_add_f32_e32 v83, v83, v116
	v_add_f32_e32 v82, v83, v82
	v_mov_b32_e32 v131, 0x358637bd
	s_mov_b32 s21, 0xf800000
	v_add_f32_dpp v82, v82, v82 quad_perm:[1,0,3,2] row_mask:0xf bank_mask:0xf bound_ctrl:1
	v_mov_b32_e32 v132, 0x260
	s_mov_b32 s24, 0x42fe0000
	v_add_f32_dpp v82, v82, v82 quad_perm:[2,3,0,1] row_mask:0xf bank_mask:0xf bound_ctrl:1
	s_add_i32 s25, s23, 0xf0
	s_mov_b32 s20, 0x40c0c00
	v_add_f32_dpp v82, v82, v82 row_half_mirror row_mask:0xf bank_mask:0xf bound_ctrl:1
	s_nop 1
	v_add_f32_dpp v82, v82, v82 row_mirror row_mask:0xf bank_mask:0xf bound_ctrl:1
	v_mov_b32_e32 v83, v82
	s_nop 1
	v_permlane16_swap_b32_e32 v82, v83
	v_add_f32_e32 v82, v82, v83
	v_mov_b32_e32 v83, v82
	s_nop 1
	v_permlane32_swap_b32_e32 v82, v83
	v_add_f32_e32 v82, v82, v83
	v_fmamk_f32 v82, v82, 0x3a800000, v131
	v_mul_f32_e32 v83, 0x4f800000, v82
	v_cmp_gt_f32_e32 vcc, s21, v82
	s_nop 1
	v_cndmask_b32_e32 v82, v82, v83, vcc
	v_sqrt_f32_e32 v83, v82
	s_nop 0
	v_add_u32_e32 v116, -1, v83
	v_fma_f32 v117, -v116, v83, v82
	v_cmp_ge_f32_e64 s[0:1], 0, v117
	v_add_u32_e32 v117, 1, v83
	s_nop 0
	v_cndmask_b32_e64 v116, v83, v116, s[0:1]
	v_fma_f32 v83, -v117, v83, v82
	v_cmp_lt_f32_e64 s[0:1], 0, v83
	s_nop 1
	v_cndmask_b32_e64 v83, v116, v117, s[0:1]
	v_mul_f32_e32 v116, 0x37800000, v83
	v_cndmask_b32_e32 v83, v83, v116, vcc
	v_cmp_class_f32_e32 vcc, v82, v132
	s_nop 1
	v_cndmask_b32_e32 v82, v83, v82, vcc
	v_div_scale_f32 v83, s[0:1], v82, v82, 1.0
	v_rcp_f32_e32 v116, v83
	s_add_i32 s0, s25, s22
	s_ashr_i32 s1, s0, 31
	v_fma_f32 v117, -v83, v116, 1.0
	v_fmac_f32_e32 v116, v117, v116
	v_div_scale_f32 v117, vcc, 1.0, v82, 1.0
	v_mul_f32_e32 v118, v117, v116
	v_fma_f32 v119, -v83, v118, v117
	v_fmac_f32_e32 v118, v119, v116
	v_fma_f32 v83, -v83, v118, v117
	v_div_fmas_f32 v83, v83, v116, v118
	v_div_fixup_f32 v82, v83, v82, 1.0
	v_pk_mul_f32 v[118:119], v[148:149], v[82:83] op_sel_hi:[1,0]
	v_pk_mul_f32 v[116:117], v[150:151], v[82:83] op_sel_hi:[1,0]
	v_pk_fma_f32 v[124:125], v[98:99], v[118:119], v[80:81]
	v_pk_mul_f32 v[118:119], v[144:145], v[82:83] op_sel_hi:[1,0]
	v_pk_fma_f32 v[128:129], v[96:97], v[116:117], v[78:79]
	v_pk_mul_f32 v[116:117], v[146:147], v[82:83] op_sel_hi:[1,0]
	v_pk_fma_f32 v[122:123], v[94:95], v[118:119], v[76:77]
	v_pk_mul_f32 v[118:119], v[142:143], v[82:83] op_sel_hi:[1,0]
	v_pk_fma_f32 v[126:127], v[92:93], v[116:117], v[74:75]
	v_pk_mul_f32 v[116:117], v[140:141], v[82:83] op_sel_hi:[1,0]
	v_pk_fma_f32 v[120:121], v[88:89], v[118:119], v[70:71]
	v_pk_mul_f32 v[118:119], v[138:139], v[82:83] op_sel_hi:[1,0]
	v_pk_mul_f32 v[82:83], v[136:137], v[82:83] op_sel_hi:[1,0]
	v_max_f32_e64 v130, |v124|, |v125|
	v_max_f32_e64 v133, |v122|, |v123|
	v_pk_fma_f32 v[116:117], v[90:91], v[116:117], v[72:73]
	v_pk_fma_f32 v[82:83], v[86:87], v[82:83], v[60:61]
	v_max3_f32 v130, |v128|, |v129|, v130
	v_max3_f32 v133, |v126|, |v127|, v133
	v_pk_fma_f32 v[118:119], v[84:85], v[118:119], v[58:59]
	v_max3_f32 v130, v130, 0, v133
	v_max_f32_e64 v133, |v116|, |v117|
	v_max_f32_e64 v134, |v82|, |v83|
	v_max3_f32 v133, |v120|, |v121|, v133
	v_max3_f32 v134, |v118|, |v119|, v134
	v_max3_f32 v130, v130, v133, v134
	s_nop 1
	v_mov_b32_dpp v133, v130 quad_perm:[1,0,3,2] row_mask:0xf bank_mask:0xf bound_ctrl:1
	s_nop 0
	v_max_f32_e32 v130, v130, v133
	s_nop 1
	v_mov_b32_dpp v133, v130 quad_perm:[2,3,0,1] row_mask:0xf bank_mask:0xf bound_ctrl:1
	s_nop 0
	v_max_f32_e32 v130, v130, v133
	s_nop 1
	v_mov_b32_dpp v133, v130 row_half_mirror row_mask:0xf bank_mask:0xf bound_ctrl:1
	s_nop 0
	v_max_f32_e32 v130, v130, v133
	s_nop 1
	v_mov_b32_dpp v133, v130 row_mirror row_mask:0xf bank_mask:0xf bound_ctrl:1
	s_nop 0
	v_max_f32_e32 v130, v130, v133
	v_mov_b32_e32 v133, v130
	s_nop 1
	v_permlane16_swap_b32_e32 v130, v133
	s_nop 0
	s_nop 0
	v_max_f32_e32 v130, v130, v133
	v_mov_b32_e32 v133, v130
	s_nop 1
	v_permlane32_swap_b32_e32 v130, v133
	s_nop 0
	s_nop 0
	v_max_f32_e32 v133, v130, v133
	v_div_scale_f32 v130, s[18:19], v133, v133, s24
	v_rcp_f32_e32 v134, v130
	s_lshl_b64 s[18:19], s[0:1], 10
	s_add_u32 s18, s96, s18
	s_addc_u32 s19, s97, s19
	v_fma_f32 v135, -v130, v134, 1.0
	v_fmac_f32_e32 v134, v135, v134
	v_div_scale_f32 v135, vcc, s24, v133, s24
	v_mul_f32_e32 v136, v135, v134
	v_fma_f32 v137, -v130, v136, v135
	v_fmac_f32_e32 v136, v137, v134
	v_fma_f32 v130, -v130, v136, v135
	v_div_fmas_f32 v130, v130, v134, v136
	v_div_fixup_f32 v130, v130, v133, s24
	v_cmp_lt_f32_e32 vcc, 0, v133
	s_nop 1
	v_cndmask_b32_e32 v134, 0, v130, vcc
	v_mul_f32_e32 v136, v134, v129
	v_mul_f32_e32 v135, v134, v128
	v_rndne_f32_e32 v136, v136
	v_mul_f32_e32 v137, v134, v124
	v_mul_f32_e32 v138, v134, v125
	v_rndne_f32_e32 v135, v135
	v_rndne_f32_e32 v137, v137
	v_cvt_i32_f32_e32 v136, v136
	v_rndne_f32_e32 v138, v138
	v_cvt_i32_f32_e32 v135, v135
	v_cvt_i32_f32_sdwa v137, v137 dst_sel:WORD_1 dst_unused:UNUSED_PAD src0_sel:DWORD
	v_cvt_i32_f32_e32 v138, v138
	v_lshlrev_b32_e32 v136, 8, v136
	v_and_b32_e32 v136, 0xff00, v136
	v_and_b32_e32 v137, 0xff0000, v137
	v_perm_b32 v135, v138, v135, s20
	v_lshlrev_b32_e32 v130, 2, v174
	v_or3_b32 v135, v135, v136, v137
	v_mul_f32_e32 v136, v134, v127
	global_store_dword v130, v135, s[18:19]
	v_mul_f32_e32 v135, v134, v126
	v_rndne_f32_e32 v136, v136
	v_mul_f32_e32 v137, v134, v122
	v_mul_f32_e32 v138, v134, v123
	v_rndne_f32_e32 v135, v135
	v_rndne_f32_e32 v137, v137
	v_rndne_f32_e32 v138, v138
	v_cvt_i32_f32_e32 v136, v136
	v_cvt_i32_f32_e32 v135, v135
	v_cvt_i32_f32_sdwa v137, v137 dst_sel:WORD_1 dst_unused:UNUSED_PAD src0_sel:DWORD
	v_cvt_i32_f32_e32 v138, v138
	v_lshlrev_b32_e32 v136, 8, v136
	v_and_b32_e32 v136, 0xff00, v136
	v_and_b32_e32 v137, 0xff0000, v137
	v_perm_b32 v135, v138, v135, s20
	v_or3_b32 v135, v135, v136, v137
	v_mul_f32_e32 v136, v134, v121
	global_store_dword v130, v135, s[18:19] offset:256
	v_mul_f32_e32 v135, v134, v120
	v_rndne_f32_e32 v136, v136
	v_mul_f32_e32 v137, v134, v116
	v_mul_f32_e32 v138, v134, v117
	v_rndne_f32_e32 v135, v135
	v_rndne_f32_e32 v137, v137
	v_rndne_f32_e32 v138, v138
	v_cvt_i32_f32_e32 v136, v136
	v_cvt_i32_f32_e32 v135, v135
	v_cvt_i32_f32_sdwa v137, v137 dst_sel:WORD_1 dst_unused:UNUSED_PAD src0_sel:DWORD
	v_cvt_i32_f32_e32 v138, v138
	v_lshlrev_b32_e32 v136, 8, v136
	v_and_b32_e32 v136, 0xff00, v136
	v_and_b32_e32 v137, 0xff0000, v137
	v_perm_b32 v135, v138, v135, s20
	v_or3_b32 v135, v135, v136, v137
	v_mul_f32_e32 v136, v134, v119
	global_store_dword v130, v135, s[18:19] offset:512
	v_mul_f32_e32 v135, v134, v118
	v_rndne_f32_e32 v136, v136
	v_mul_f32_e32 v137, v134, v82
	v_mul_f32_e32 v134, v134, v83
	v_rndne_f32_e32 v135, v135
	v_rndne_f32_e32 v137, v137
	v_rndne_f32_e32 v134, v134
	v_cvt_i32_f32_e32 v136, v136
	v_cvt_i32_f32_e32 v135, v135
	v_cvt_i32_f32_sdwa v137, v137 dst_sel:WORD_1 dst_unused:UNUSED_PAD src0_sel:DWORD
	v_cvt_i32_f32_e32 v134, v134
	v_lshlrev_b32_e32 v136, 8, v136
	v_and_b32_e32 v136, 0xff00, v136
	v_and_b32_e32 v137, 0xff0000, v137
	v_perm_b32 v134, v134, v135, s20
	v_or3_b32 v134, v134, v136, v137
	global_store_dword v130, v134, s[18:19] offset:768
	s_and_saveexec_b64 s[18:19], s[14:15]
	s_cbranch_execz .LBB0_2995
	s_lshl_b32 s25, s25, 2
	s_add_i32 s25, s25, 0
	s_add_i32 s25, s25, 0x23500
	s_lshl_b64 s[0:1], s[0:1], 2
	s_add_u32 s0, s82, s0
	s_addc_u32 s1, s83, s1
	v_mov_b32_e32 v134, 0
	v_mul_f32_e32 v133, 0x3c010204, v133
	global_store_dword v134, v133, s[0:1]
	v_mov_b32_e32 v134, s25
	ds_write_b32 v134, v133
.LBB0_2995:
	s_or_b64 exec, exec, s[18:19]
	v_cvt_pk_bf16_f32 v134, v128, v129
	v_cvt_pk_bf16_f32 v135, v124, v125
	v_lshlrev_b32_e32 v136, 16, v134
	v_and_b32_e32 v137, 0xffff0000, v134
	v_pk_add_f32 v[128:129], v[128:129], v[136:137] neg_lo:[0,1] neg_hi:[0,1]
	v_lshlrev_b32_e32 v136, 16, v135
	v_and_b32_e32 v137, 0xffff0000, v135
	v_pk_add_f32 v[124:125], v[124:125], v[136:137] neg_lo:[0,1] neg_hi:[0,1]
	v_cvt_pk_bf16_f32 v128, v128, v129
	v_cvt_pk_bf16_f32 v129, v124, v125
	v_cvt_pk_bf16_f32 v124, v126, v127
	v_cvt_pk_bf16_f32 v125, v122, v123
	ds_write2st64_b64 v156, v[134:135], v[124:125] offset1:1
	v_lshlrev_b32_e32 v134, 16, v124
	v_and_b32_e32 v135, 0xffff0000, v124
	v_pk_add_f32 v[126:127], v[126:127], v[134:135] neg_lo:[0,1] neg_hi:[0,1]
	s_nop 0
	v_cvt_pk_bf16_f32 v124, v126, v127
	v_lshlrev_b32_e32 v126, 16, v125
	v_and_b32_e32 v127, 0xffff0000, v125
	v_pk_add_f32 v[122:123], v[122:123], v[126:127] neg_lo:[0,1] neg_hi:[0,1]
	v_add_u32_e32 v126, 0x100, v156
	v_cvt_pk_bf16_f32 v125, v122, v123
	v_cvt_pk_bf16_f32 v122, v120, v121
	ds_write2st64_b64 v126, v[128:129], v[124:125] offset0:64 offset1:65
	v_cvt_pk_bf16_f32 v123, v116, v117
	v_lshlrev_b32_e32 v124, 16, v122
	v_and_b32_e32 v125, 0xffff0000, v122
	v_pk_add_f32 v[120:121], v[120:121], v[124:125] neg_lo:[0,1] neg_hi:[0,1]
	v_lshlrev_b32_e32 v124, 16, v123
	v_and_b32_e32 v125, 0xffff0000, v123
	v_pk_add_f32 v[116:117], v[116:117], v[124:125] neg_lo:[0,1] neg_hi:[0,1]
	v_cvt_pk_bf16_f32 v120, v120, v121
	v_cvt_pk_bf16_f32 v121, v116, v117
	v_cvt_pk_bf16_f32 v116, v118, v119
	v_cvt_pk_bf16_f32 v117, v82, v83
	ds_write2st64_b64 v156, v[122:123], v[116:117] offset0:2 offset1:3
	v_lshlrev_b32_e32 v122, 16, v116
	v_and_b32_e32 v123, 0xffff0000, v116
	v_pk_add_f32 v[118:119], v[118:119], v[122:123] neg_lo:[0,1] neg_hi:[0,1]
	v_mul_f32_e32 v122, v113, v113
	v_cvt_pk_bf16_f32 v116, v118, v119
	v_mul_f32_e32 v119, v115, v115
	v_fmac_f32_e32 v119, v114, v114
	v_fmac_f32_e32 v122, v112, v112
	v_add_f32_e32 v119, v119, v122
	v_mul_f32_e32 v122, v111, v111
	v_mul_f32_e32 v123, v109, v109
	v_fmac_f32_e32 v122, v110, v110
	v_fmac_f32_e32 v123, v108, v108
	v_add_f32_e32 v122, v122, v123
	v_add_f32_e32 v119, v119, v122
	v_mul_f32_e32 v122, v107, v107
	v_mul_f32_e32 v123, v105, v105
	v_fmac_f32_e32 v122, v106, v106
	v_fmac_f32_e32 v123, v104, v104
	v_add_f32_e32 v122, v122, v123
	v_add_f32_e32 v119, v122, v119
	v_mul_f32_e32 v122, v103, v103
	v_mul_f32_e32 v123, v101, v101
	v_fmac_f32_e32 v122, v102, v102
	v_fmac_f32_e32 v123, v100, v100
	v_add_f32_e32 v122, v122, v123
	v_add_f32_e32 v119, v122, v119
	v_lshlrev_b32_e32 v118, 16, v117
	s_nop 0
	v_add_f32_dpp v119, v119, v119 quad_perm:[1,0,3,2] row_mask:0xf bank_mask:0xf bound_ctrl:1
	s_nop 1
	v_add_f32_dpp v119, v119, v119 quad_perm:[2,3,0,1] row_mask:0xf bank_mask:0xf bound_ctrl:1
	s_nop 1
	v_add_f32_dpp v119, v119, v119 row_half_mirror row_mask:0xf bank_mask:0xf bound_ctrl:1
	s_nop 1
	v_add_f32_dpp v119, v119, v119 row_mirror row_mask:0xf bank_mask:0xf bound_ctrl:1
	v_mov_b32_e32 v122, v119
	s_nop 1
	v_permlane16_swap_b32_e32 v119, v122
	v_add_f32_e32 v119, v119, v122
	v_mov_b32_e32 v122, v119
	s_nop 1
	v_permlane32_swap_b32_e32 v119, v122
	v_add_f32_e32 v119, v119, v122
	v_fmac_f32_e32 v131, 0x3a800000, v119
	v_mul_f32_e32 v119, 0x4f800000, v131
	v_cmp_gt_f32_e32 vcc, s21, v131
	s_add_i32 s21, s23, 0xf1
	s_nop 0
	v_cndmask_b32_e32 v122, v131, v119, vcc
	v_sqrt_f32_e32 v123, v122
	v_and_b32_e32 v119, 0xffff0000, v117
	v_pk_add_f32 v[82:83], v[82:83], v[118:119] neg_lo:[0,1] neg_hi:[0,1]
	s_nop 0
	v_cvt_pk_bf16_f32 v117, v82, v83
	v_add_u32_e32 v82, -1, v123
	v_fma_f32 v83, -v82, v123, v122
	v_cmp_ge_f32_e64 s[0:1], 0, v83
	v_add_u32_e32 v83, 1, v123
	v_fma_f32 v118, -v83, v123, v122
	v_cndmask_b32_e64 v82, v123, v82, s[0:1]
	v_cmp_lt_f32_e64 s[0:1], 0, v118
	ds_write2st64_b64 v126, v[120:121], v[116:117] offset0:66 offset1:67
	s_nop 0
	v_cndmask_b32_e64 v82, v82, v83, s[0:1]
	v_mul_f32_e32 v83, 0x37800000, v82
	v_cndmask_b32_e32 v82, v82, v83, vcc
	v_cmp_class_f32_e32 vcc, v122, v132
	s_nop 1
	v_cndmask_b32_e32 v82, v82, v122, vcc
	v_div_scale_f32 v83, s[0:1], v82, v82, 1.0
	v_rcp_f32_e32 v118, v83
	s_add_i32 s0, s21, s22
	s_ashr_i32 s1, s0, 31
	v_fma_f32 v116, -v83, v118, 1.0
	v_fmac_f32_e32 v118, v116, v118
	v_div_scale_f32 v116, vcc, 1.0, v82, 1.0
	v_mul_f32_e32 v117, v116, v118
	v_fma_f32 v119, -v83, v117, v116
	v_fmac_f32_e32 v117, v119, v118
	v_fma_f32 v83, -v83, v117, v116
	v_div_fmas_f32 v83, v83, v118, v117
	v_div_fixup_f32 v82, v83, v82, 1.0
	v_pk_mul_f32 v[114:115], v[114:115], v[82:83] op_sel_hi:[1,0]
	v_pk_mul_f32 v[112:113], v[112:113], v[82:83] op_sel_hi:[1,0]
	v_pk_fma_f32 v[78:79], v[96:97], v[114:115], v[78:79]
	v_pk_mul_f32 v[96:97], v[110:111], v[82:83] op_sel_hi:[1,0]
	v_pk_fma_f32 v[80:81], v[98:99], v[112:113], v[80:81]
	v_pk_mul_f32 v[98:99], v[108:109], v[82:83] op_sel_hi:[1,0]
	v_pk_fma_f32 v[74:75], v[92:93], v[96:97], v[74:75]
	v_pk_mul_f32 v[92:93], v[106:107], v[82:83] op_sel_hi:[1,0]
	v_pk_fma_f32 v[76:77], v[94:95], v[98:99], v[76:77]
	v_pk_mul_f32 v[94:95], v[104:105], v[82:83] op_sel_hi:[1,0]
	v_pk_fma_f32 v[70:71], v[88:89], v[92:93], v[70:71]
	v_pk_mul_f32 v[88:89], v[102:103], v[82:83] op_sel_hi:[1,0]
	v_pk_mul_f32 v[82:83], v[100:101], v[82:83] op_sel_hi:[1,0]
	v_pk_fma_f32 v[72:73], v[90:91], v[94:95], v[72:73]
	v_pk_fma_f32 v[60:61], v[86:87], v[82:83], v[60:61]
	v_max_f32_e64 v82, |v80|, |v81|
	v_max_f32_e64 v83, |v76|, |v77|
	v_max3_f32 v82, |v78|, |v79|, v82
	v_max3_f32 v83, |v74|, |v75|, v83
	v_pk_fma_f32 v[58:59], v[84:85], v[88:89], v[58:59]
	v_max3_f32 v82, v82, 0, v83
	v_max_f32_e64 v83, |v72|, |v73|
	v_max_f32_e64 v84, |v60|, |v61|
	v_max3_f32 v83, |v70|, |v71|, v83
	v_max3_f32 v84, |v58|, |v59|, v84
	v_max3_f32 v82, v82, v83, v84
	s_nop 1
	v_mov_b32_dpp v83, v82 quad_perm:[1,0,3,2] row_mask:0xf bank_mask:0xf bound_ctrl:1
	s_nop 0
	v_max_f32_e32 v82, v82, v83
	s_nop 1
	v_mov_b32_dpp v83, v82 quad_perm:[2,3,0,1] row_mask:0xf bank_mask:0xf bound_ctrl:1
	s_nop 0
	v_max_f32_e32 v82, v82, v83
	s_nop 1
	v_mov_b32_dpp v83, v82 row_half_mirror row_mask:0xf bank_mask:0xf bound_ctrl:1
	s_nop 0
	v_max_f32_e32 v82, v82, v83
	s_nop 1
	v_mov_b32_dpp v83, v82 row_mirror row_mask:0xf bank_mask:0xf bound_ctrl:1
	s_nop 0
	v_max_f32_e32 v82, v82, v83
	v_mov_b32_e32 v83, v82
	s_nop 1
	v_permlane16_swap_b32_e32 v82, v83
	s_nop 0
	s_nop 0
	v_max_f32_e32 v82, v82, v83
	v_mov_b32_e32 v83, v82
	s_nop 1
	v_permlane32_swap_b32_e32 v82, v83
	s_nop 0
	s_nop 0
	v_max_f32_e32 v82, v82, v83
	v_div_scale_f32 v83, s[18:19], v82, v82, s24
	v_rcp_f32_e32 v84, v83
	s_lshl_b64 s[18:19], s[0:1], 10
	s_add_u32 s18, s96, s18
	s_addc_u32 s19, s97, s19
	v_fma_f32 v85, -v83, v84, 1.0
	v_fmac_f32_e32 v84, v85, v84
	v_div_scale_f32 v85, vcc, s24, v82, s24
	v_mul_f32_e32 v86, v85, v84
	v_fma_f32 v87, -v83, v86, v85
	v_fmac_f32_e32 v86, v87, v84
	v_fma_f32 v83, -v83, v86, v85
	v_div_fmas_f32 v83, v83, v84, v86
	v_div_fixup_f32 v83, v83, v82, s24
	v_cmp_lt_f32_e32 vcc, 0, v82
	s_nop 1
	v_cndmask_b32_e32 v83, 0, v83, vcc
	v_mul_f32_e32 v85, v83, v79
	v_mul_f32_e32 v84, v83, v78
	v_rndne_f32_e32 v85, v85
	v_mul_f32_e32 v86, v83, v80
	v_mul_f32_e32 v87, v83, v81
	v_rndne_f32_e32 v84, v84
	v_rndne_f32_e32 v86, v86
	v_rndne_f32_e32 v87, v87
	v_cvt_i32_f32_e32 v85, v85
	v_cvt_i32_f32_e32 v84, v84
	v_cvt_i32_f32_sdwa v86, v86 dst_sel:WORD_1 dst_unused:UNUSED_PAD src0_sel:DWORD
	v_cvt_i32_f32_e32 v87, v87
	v_lshlrev_b32_e32 v85, 8, v85
	v_and_b32_e32 v85, 0xff00, v85
	v_and_b32_e32 v86, 0xff0000, v86
	v_perm_b32 v84, v87, v84, s20
	v_or3_b32 v84, v84, v85, v86
	v_mul_f32_e32 v85, v83, v75
	global_store_dword v130, v84, s[18:19]
	v_mul_f32_e32 v84, v83, v74
	v_rndne_f32_e32 v85, v85
	v_mul_f32_e32 v86, v83, v76
	v_mul_f32_e32 v87, v83, v77
	v_rndne_f32_e32 v84, v84
	v_rndne_f32_e32 v86, v86
	v_rndne_f32_e32 v87, v87
	v_cvt_i32_f32_e32 v85, v85
	v_cvt_i32_f32_e32 v84, v84
	v_cvt_i32_f32_sdwa v86, v86 dst_sel:WORD_1 dst_unused:UNUSED_PAD src0_sel:DWORD
	v_cvt_i32_f32_e32 v87, v87
	v_lshlrev_b32_e32 v85, 8, v85
	v_and_b32_e32 v85, 0xff00, v85
	v_and_b32_e32 v86, 0xff0000, v86
	v_perm_b32 v84, v87, v84, s20
	v_or3_b32 v84, v84, v85, v86
	v_mul_f32_e32 v85, v83, v71
	global_store_dword v130, v84, s[18:19] offset:256
	v_mul_f32_e32 v84, v83, v70
	v_rndne_f32_e32 v85, v85
	v_mul_f32_e32 v86, v83, v72
	v_mul_f32_e32 v87, v83, v73
	v_rndne_f32_e32 v84, v84
	v_rndne_f32_e32 v86, v86
	v_rndne_f32_e32 v87, v87
	v_cvt_i32_f32_e32 v85, v85
	v_cvt_i32_f32_e32 v84, v84
	v_cvt_i32_f32_sdwa v86, v86 dst_sel:WORD_1 dst_unused:UNUSED_PAD src0_sel:DWORD
	v_cvt_i32_f32_e32 v87, v87
	v_lshlrev_b32_e32 v85, 8, v85
	v_and_b32_e32 v85, 0xff00, v85
	v_and_b32_e32 v86, 0xff0000, v86
	v_perm_b32 v84, v87, v84, s20
	v_or3_b32 v84, v84, v85, v86
	v_mul_f32_e32 v85, v83, v59
	global_store_dword v130, v84, s[18:19] offset:512
	v_mul_f32_e32 v84, v83, v58
	v_rndne_f32_e32 v85, v85
	v_mul_f32_e32 v86, v83, v60
	v_mul_f32_e32 v83, v83, v61
	v_rndne_f32_e32 v84, v84
	v_rndne_f32_e32 v86, v86
	v_rndne_f32_e32 v83, v83
	v_cvt_i32_f32_e32 v85, v85
	v_cvt_i32_f32_e32 v84, v84
	v_cvt_i32_f32_sdwa v86, v86 dst_sel:WORD_1 dst_unused:UNUSED_PAD src0_sel:DWORD
	v_cvt_i32_f32_e32 v83, v83
	v_lshlrev_b32_e32 v85, 8, v85
	v_and_b32_e32 v85, 0xff00, v85
	v_and_b32_e32 v86, 0xff0000, v86
	v_perm_b32 v83, v83, v84, s20
	v_or3_b32 v83, v83, v85, v86
	global_store_dword v130, v83, s[18:19] offset:768
	s_and_saveexec_b64 s[18:19], s[14:15]
	s_cbranch_execz .LBB0_2997
	s_lshl_b32 s14, s21, 2
	s_add_i32 s14, s14, 0
	s_add_i32 s14, s14, 0x23500
	s_lshl_b64 s[0:1], s[0:1], 2
	s_add_u32 s0, s82, s0
	s_addc_u32 s1, s83, s1
	v_mov_b32_e32 v83, 0
	v_mul_f32_e32 v82, 0x3c010204, v82
	global_store_dword v83, v82, s[0:1]
	v_mov_b32_e32 v83, s14
	ds_write_b32 v83, v82
.LBB0_2997:
	s_or_b64 exec, exec, s[18:19]
	v_cvt_pk_bf16_f32 v82, v78, v79
	v_cvt_pk_bf16_f32 v83, v80, v81
	v_lshlrev_b32_e32 v84, 16, v82
	v_and_b32_e32 v85, 0xffff0000, v82
	v_pk_add_f32 v[78:79], v[78:79], v[84:85] neg_lo:[0,1] neg_hi:[0,1]
	v_lshlrev_b32_e32 v84, 16, v83
	v_and_b32_e32 v85, 0xffff0000, v83
	v_pk_add_f32 v[80:81], v[80:81], v[84:85] neg_lo:[0,1] neg_hi:[0,1]
	v_cvt_pk_bf16_f32 v78, v78, v79
	v_cvt_pk_bf16_f32 v79, v80, v81
	v_cvt_pk_bf16_f32 v80, v74, v75
	v_cvt_pk_bf16_f32 v81, v76, v77
	v_add_u32_e32 v84, 16, v156
	ds_write2st64_b64 v84, v[82:83], v[80:81] offset0:4 offset1:5
	v_lshlrev_b32_e32 v82, 16, v80
	v_and_b32_e32 v83, 0xffff0000, v80
	v_lshlrev_b32_e32 v80, 16, v81
	v_and_b32_e32 v81, 0xffff0000, v81
	v_pk_add_f32 v[74:75], v[74:75], v[82:83] neg_lo:[0,1] neg_hi:[0,1]
	v_pk_add_f32 v[76:77], v[76:77], v[80:81] neg_lo:[0,1] neg_hi:[0,1]
	v_cvt_pk_bf16_f32 v74, v74, v75
	v_cvt_pk_bf16_f32 v75, v76, v77
	v_add_u32_e32 v80, 0x110, v156
	ds_write2st64_b64 v80, v[78:79], v[74:75] offset0:68 offset1:69
	v_cvt_pk_bf16_f32 v74, v70, v71
	v_cvt_pk_bf16_f32 v75, v72, v73
	v_lshlrev_b32_e32 v76, 16, v74
	v_and_b32_e32 v77, 0xffff0000, v74
	v_pk_add_f32 v[70:71], v[70:71], v[76:77] neg_lo:[0,1] neg_hi:[0,1]
	v_lshlrev_b32_e32 v76, 16, v75
	v_and_b32_e32 v77, 0xffff0000, v75
	v_pk_add_f32 v[72:73], v[72:73], v[76:77] neg_lo:[0,1] neg_hi:[0,1]
	v_cvt_pk_bf16_f32 v70, v70, v71
	v_cvt_pk_bf16_f32 v71, v72, v73
	v_cvt_pk_bf16_f32 v72, v58, v59
	v_cvt_pk_bf16_f32 v73, v60, v61
	ds_write2st64_b64 v84, v[74:75], v[72:73] offset0:6 offset1:7
	v_lshlrev_b32_e32 v74, 16, v72
	v_and_b32_e32 v75, 0xffff0000, v72
	v_lshlrev_b32_e32 v72, 16, v73
	v_and_b32_e32 v73, 0xffff0000, v73
	v_pk_add_f32 v[58:59], v[58:59], v[74:75] neg_lo:[0,1] neg_hi:[0,1]
	v_pk_add_f32 v[60:61], v[60:61], v[72:73] neg_lo:[0,1] neg_hi:[0,1]
	v_cvt_pk_bf16_f32 v58, v58, v59
	v_cvt_pk_bf16_f32 v59, v60, v61
	ds_write2st64_b64 v80, v[70:71], v[58:59] offset0:70 offset1:71
	s_waitcnt lgkmcnt(0)
	s_barrier
	ds_read_b128 v[58:61], v162
	ds_read_b128 v[70:73], v162 offset:64
	s_waitcnt lgkmcnt(1)
	v_mfma_f32_16x16x32_bf16 v[74:77], v[58:61], v[2:5], 0
	ds_read_b128 v[82:85], v162 offset:33024
	ds_read_b128 v[86:89], v162 offset:33088
	v_mfma_f32_16x16x32_bf16 v[78:81], v[58:61], v[6:9], 0
	s_waitcnt lgkmcnt(1)
	v_mfma_f32_16x16x32_bf16 v[2:5], v[82:85], v[2:5], v[74:77]
	v_mfma_f32_16x16x32_bf16 v[6:9], v[82:85], v[6:9], v[78:81]
	v_mfma_f32_16x16x32_bf16 v[2:5], v[58:61], v[10:13], v[2:5]
	v_mfma_f32_16x16x32_bf16 v[6:9], v[58:61], v[14:17], v[6:9]
	ds_read_b128 v[10:13], v162 offset:128
	ds_read_b128 v[14:17], v162 offset:192
	v_mfma_f32_16x16x32_bf16 v[2:5], v[70:73], v[18:21], v[2:5]
	v_mfma_f32_16x16x32_bf16 v[6:9], v[70:73], v[22:25], v[6:9]
	s_waitcnt lgkmcnt(2)
	v_mfma_f32_16x16x32_bf16 v[2:5], v[86:89], v[18:21], v[2:5]
	v_mfma_f32_16x16x32_bf16 v[6:9], v[86:89], v[22:25], v[6:9]
	ds_read_b128 v[18:21], v162 offset:33152
	ds_read_b128 v[22:25], v162 offset:33216
	v_mfma_f32_16x16x32_bf16 v[2:5], v[70:73], v[26:29], v[2:5]
	v_mfma_f32_16x16x32_bf16 v[6:9], v[70:73], v[34:37], v[6:9]
	s_waitcnt lgkmcnt(3)
	v_mfma_f32_16x16x32_bf16 v[2:5], v[10:13], v[30:33], v[2:5]
	v_mfma_f32_16x16x32_bf16 v[6:9], v[10:13], v[38:41], v[6:9]
	s_waitcnt lgkmcnt(1)
	v_mfma_f32_16x16x32_bf16 v[2:5], v[18:21], v[30:33], v[2:5]
	v_mfma_f32_16x16x32_bf16 v[6:9], v[18:21], v[38:41], v[6:9]
	v_mfma_f32_16x16x32_bf16 v[2:5], v[10:13], v[42:45], v[2:5]
	v_mfma_f32_16x16x32_bf16 v[6:9], v[10:13], v[46:49], v[6:9]
	v_mfma_f32_16x16x32_bf16 v[2:5], v[14:17], v[50:53], v[2:5]
	v_mfma_f32_16x16x32_bf16 v[6:9], v[14:17], v[54:57], v[6:9]
	s_waitcnt lgkmcnt(0)
	v_mfma_f32_16x16x32_bf16 v[2:5], v[22:25], v[50:53], v[2:5]
	v_mfma_f32_16x16x32_bf16 v[6:9], v[22:25], v[54:57], v[6:9]
	v_mfma_f32_16x16x32_bf16 v[2:5], v[14:17], v[62:65], v[2:5]
	v_mfma_f32_16x16x32_bf16 v[6:9], v[14:17], v[66:69], v[6:9]
	s_nop 7
	ds_write2_b32 v155, v2, v6 offset1:16
	ds_write2_b32 v155, v3, v7 offset0:32 offset1:48
	ds_write2_b32 v155, v4, v8 offset0:64 offset1:80
	ds_write2_b32 v155, v5, v9 offset0:96 offset1:112
	s_waitcnt lgkmcnt(0)
	s_barrier
	ds_read2st64_b32 v[2:3], v154 offset1:8
	ds_read2st64_b32 v[4:5], v154 offset0:16 offset1:24
	ds_read2st64_b32 v[6:7], v154 offset0:32 offset1:40
	s_waitcnt lgkmcnt(2)
	v_add_f32_e32 v1, v1, v2
	v_add_f32_e32 v1, v1, v3
	ds_read2st64_b32 v[2:3], v154 offset0:48 offset1:56
	s_waitcnt lgkmcnt(2)
	v_add_f32_e32 v1, v1, v4
	v_add_f32_e32 v1, v1, v5
	s_waitcnt lgkmcnt(1)
	v_add_f32_e32 v1, v1, v6
	v_add_f32_e32 v1, v1, v7
	s_waitcnt lgkmcnt(0)
	v_add_f32_e32 v1, v1, v2
	v_add_f32_e32 v3, v1, v3
	v_mov_b32_e32 v7, 0xff800000
	s_nop 0
	v_mov_b32_dpp v1, v3 quad_perm:[1,0,3,2] row_mask:0xf bank_mask:0xf bound_ctrl:1
	s_nop 0
	v_max_f32_e32 v1, v3, v1
	s_nop 1
	v_mov_b32_dpp v2, v1 quad_perm:[2,3,0,1] row_mask:0xf bank_mask:0xf bound_ctrl:1
	s_nop 0
	v_max_f32_e32 v1, v1, v2
	s_nop 1
	v_mov_b32_dpp v2, v1 row_half_mirror row_mask:0xf bank_mask:0xf bound_ctrl:1
	s_nop 0
	v_max_f32_e32 v1, v1, v2
	s_nop 1
	v_mov_b32_dpp v2, v1 row_mirror row_mask:0xf bank_mask:0xf bound_ctrl:1
	s_nop 0
	v_max_f32_e32 v1, v1, v2
	v_mov_b32_e32 v2, v1
	s_nop 1
	v_permlane16_swap_b32_e32 v1, v2
	s_nop 0
	s_nop 0
	v_max_f32_e32 v2, v1, v2
	v_cmp_eq_f32_e32 vcc, v3, v2
	s_nop 1
	v_mov_b32_e32 v1, vcc_hi
	v_mov_b32_e32 v4, vcc_lo
	v_cndmask_b32_e64 v1, v1, v4, s[10:11]
	v_ffbl_b32_e32 v1, v1
	v_cmp_ne_u32_e32 vcc, v178, v1
	s_nop 1
	v_cndmask_b32_e32 v4, v7, v3, vcc
	s_nop 1
	v_mov_b32_dpp v3, v4 quad_perm:[1,0,3,2] row_mask:0xf bank_mask:0xf bound_ctrl:1
	s_nop 0
	v_max_f32_e32 v3, v4, v3
	s_nop 1
	v_mov_b32_dpp v5, v3 quad_perm:[2,3,0,1] row_mask:0xf bank_mask:0xf bound_ctrl:1
	s_nop 0
	v_max_f32_e32 v3, v3, v5
	s_nop 1
	v_mov_b32_dpp v5, v3 row_half_mirror row_mask:0xf bank_mask:0xf bound_ctrl:1
	s_nop 0
	v_max_f32_e32 v3, v3, v5
	s_nop 1
	v_mov_b32_dpp v5, v3 row_mirror row_mask:0xf bank_mask:0xf bound_ctrl:1
	s_nop 0
	v_max_f32_e32 v3, v3, v5
	v_mov_b32_e32 v5, v3
	s_nop 1
	v_permlane16_swap_b32_e32 v3, v5
	s_nop 0
	s_nop 0
	v_max_f32_e32 v5, v3, v5
	v_cmp_eq_f32_e32 vcc, v4, v5
	s_nop 1
	v_mov_b32_e32 v3, vcc_hi
	v_mov_b32_e32 v6, vcc_lo
	v_cndmask_b32_e64 v3, v3, v6, s[10:11]
	v_ffbl_b32_e32 v3, v3
	v_cmp_ne_u32_e32 vcc, v178, v3
	s_nop 1
	v_cndmask_b32_e32 v8, v7, v4, vcc
	s_nop 1
	v_mov_b32_dpp v4, v8 quad_perm:[1,0,3,2] row_mask:0xf bank_mask:0xf bound_ctrl:1
	s_nop 0
	v_max_f32_e32 v4, v8, v4
	s_nop 1
	v_mov_b32_dpp v6, v4 quad_perm:[2,3,0,1] row_mask:0xf bank_mask:0xf bound_ctrl:1
	s_nop 0
	v_max_f32_e32 v4, v4, v6
	s_nop 1
	v_mov_b32_dpp v6, v4 row_half_mirror row_mask:0xf bank_mask:0xf bound_ctrl:1
	s_nop 0
	v_max_f32_e32 v4, v4, v6
	s_nop 1
	v_mov_b32_dpp v6, v4 row_mirror row_mask:0xf bank_mask:0xf bound_ctrl:1
	s_nop 0
	v_max_f32_e32 v4, v4, v6
	v_mov_b32_e32 v6, v4
	s_nop 1
	v_permlane16_swap_b32_e32 v4, v6
	s_nop 0
	s_nop 0
	v_max_f32_e32 v6, v4, v6
	v_cmp_eq_f32_e32 vcc, v8, v6
	s_nop 1
	v_mov_b32_e32 v4, vcc_hi
	v_mov_b32_e32 v9, vcc_lo
	v_cndmask_b32_e64 v4, v4, v9, s[10:11]
	v_ffbl_b32_e32 v4, v4
	v_cmp_ne_u32_e32 vcc, v178, v4
	s_nop 1
	v_cndmask_b32_e32 v8, v7, v8, vcc
	s_nop 1
	v_mov_b32_dpp v7, v8 quad_perm:[1,0,3,2] row_mask:0xf bank_mask:0xf bound_ctrl:1
	s_nop 0
	v_max_f32_e32 v7, v8, v7
	s_nop 1
	v_mov_b32_dpp v9, v7 quad_perm:[2,3,0,1] row_mask:0xf bank_mask:0xf bound_ctrl:1
	s_nop 0
	v_max_f32_e32 v7, v7, v9
	s_nop 1
	v_mov_b32_dpp v9, v7 row_half_mirror row_mask:0xf bank_mask:0xf bound_ctrl:1
	s_nop 0
	v_max_f32_e32 v7, v7, v9
	s_nop 1
	v_mov_b32_dpp v9, v7 row_mirror row_mask:0xf bank_mask:0xf bound_ctrl:1
	s_nop 0
	v_max_f32_e32 v7, v7, v9
	v_mov_b32_e32 v9, v7
	s_nop 1
	v_permlane16_swap_b32_e32 v7, v9
	s_nop 0
	s_nop 0
	v_max_f32_e32 v7, v7, v9
	v_cmp_eq_f32_e64 s[0:1], v8, v7
	s_and_saveexec_b64 s[14:15], s[12:13]
	s_cbranch_execz .LBB0_2999
	v_sub_f32_e32 v5, v5, v2
	v_mul_f32_e32 v5, 0x3fb8aa3b, v5
	v_sub_f32_e32 v6, v6, v2
	v_exp_f32_e32 v5, v5
	v_mul_f32_e32 v6, 0x3fb8aa3b, v6
	v_sub_f32_e32 v2, v7, v2
	v_exp_f32_e32 v6, v6
	v_mul_f32_e32 v2, 0x3fb8aa3b, v2
	v_exp_f32_e32 v2, v2
	v_add_f32_e32 v7, 1.0, v5
	v_add_f32_e32 v7, v7, v6
	v_add_f32_e32 v7, v7, v2
	v_div_scale_f32 v8, s[12:13], v7, v7, 1.0
	v_rcp_f32_e32 v9, v8
	v_cndmask_b32_e64 v2, v2, v6, s[8:9]
	v_cndmask_b32_e64 v2, v2, v5, s[6:7]
	v_cndmask_b32_e64 v2, v2, 1.0, s[4:5]
	v_fma_f32 v10, -v8, v9, 1.0
	v_fmac_f32_e32 v9, v10, v9
	v_div_scale_f32 v10, vcc, 1.0, v7, 1.0
	v_mul_f32_e32 v11, v10, v9
	v_fma_f32 v12, -v8, v11, v10
	v_fmac_f32_e32 v11, v12, v9
	v_fma_f32 v8, -v8, v11, v10
	v_div_fmas_f32 v8, v8, v9, v11
	v_div_fixup_f32 v7, v8, v7, 1.0
	v_mov_b32_e32 v8, s1
	v_mov_b32_e32 v9, s0
	v_cndmask_b32_e64 v8, v8, v9, s[10:11]
	v_ffbl_b32_e32 v8, v8
	v_cndmask_b32_e64 v4, v8, v4, s[8:9]
	v_cndmask_b32_e64 v3, v4, v3, s[6:7]
	v_cndmask_b32_e64 v1, v3, v1, s[4:5]
	v_lshl_add_u32 v3, v1, 2, 0
	v_add_u32_e32 v3, 0x20400, v3
	v_mov_b32_e32 v4, 1
	ds_add_rtn_u32 v3, v3, v4
	v_lshl_add_u32 v4, v152, 2, v178
	v_lshl_add_u32 v4, v4, 2, 0
	v_add_u32_e32 v5, 0x21400, v4
	ds_write_b32 v5, v1
	v_add_u32_e32 v1, 0x22400, v4
	v_mul_f32_e32 v2, v7, v2
	s_waitcnt lgkmcnt(1)
	ds_write_b32 v1, v3
	v_add_u32_e32 v1, 0x23400, v4
	ds_write_b32 v1, v2
